# s31
# speedup vs baseline: 1.0036x; 1.0036x over previous
.LBB1_5:
	v_lshlrev_b32_e32 v67, 4, v1
	v_lshrrev_b32_e32 v1, 1, v1
	v_lshrrev_b32_e32 v69, 5, v132
	v_ashrrev_i32_e32 v66, 4, v132
	v_bitop3_b32 v1, v1, v69, 7 bitop3:0x78
	s_add_u32 s22, s24, s2
	v_lshlrev_b32_e32 v68, 7, v66
	v_lshlrev_b32_e32 v1, 4, v1
	v_and_b32_e32 v0, 8, v0
	s_addc_u32 s90, s25, s3
	v_lshl_or_b32 v201, v66, 12, v67
	v_or3_b32 v0, v68, v1, v0
	v_add_u32_e32 v100, 0x10000, v0
	v_cvt_pk_f16_f32 v1, v64, v65
	v_cvt_pk_f16_f32 v0, v62, v63
	v_cvt_pk_f16_f32 v61, v60, v61
	v_cvt_pk_f16_f32 v60, v58, v59
	ds_write2st64_b64 v100, v[0:1], v[60:61] offset1:8
	v_cvt_pk_f16_f32 v1, v56, v57
	v_cvt_pk_f16_f32 v0, v54, v55
	v_cvt_pk_f16_f32 v53, v52, v53
	v_cvt_pk_f16_f32 v52, v50, v51
	ds_write2st64_b64 v100, v[0:1], v[52:53] offset0:16 offset1:24
	v_cvt_pk_f16_f32 v1, v48, v49
	v_cvt_pk_f16_f32 v0, v46, v47
	v_cvt_pk_f16_f32 v45, v44, v45
	v_cvt_pk_f16_f32 v44, v42, v43
	ds_write2st64_b64 v100, v[0:1], v[44:45] offset0:32 offset1:40
	v_cvt_pk_f16_f32 v1, v40, v41
	v_cvt_pk_f16_f32 v0, v38, v39
	v_cvt_pk_f16_f32 v37, v36, v37
	v_cvt_pk_f16_f32 v36, v34, v35
	ds_write2st64_b64 v100, v[0:1], v[36:37] offset0:48 offset1:56
	s_add_u32 s0, s22, 0x200
	s_addc_u32 s1, s90, 0
	s_add_u32 s70, s0, 0x20000
	s_addc_u32 s71, s1, 0
	s_add_u32 s72, s0, 0x40000
	s_addc_u32 s73, s1, 0
	s_add_u32 s92, s0, 0x60000
	s_addc_u32 s93, s1, 0
	s_add_u32 s94, s0, 0x80000
	s_addc_u32 s95, s1, 0
	s_add_u32 s96, s0, 0xa0000
	s_addc_u32 s97, s1, 0
	s_add_u32 s98, s0, 0xc0000
	s_addc_u32 s99, s1, 0
	s_add_u32 s80, s0, 0xe0000
	s_addc_u32 s81, s1, 0
	global_load_dwordx4 v[70:73], v201, s[0:1] nt
	global_load_dwordx4 v[42:45], v201, s[70:71] nt
	global_load_dwordx4 v[46:49], v201, s[72:73] nt
	global_load_dwordx4 v[66:69], v201, s[92:93] nt
	global_load_dwordx4 v[62:65], v201, s[94:95] nt
	global_load_dwordx4 v[58:61], v201, s[96:97] nt
	global_load_dwordx4 v[54:57], v201, s[98:99] nt
	global_load_dwordx4 v[50:53], v201, s[80:81] nt
	s_waitcnt vmcnt(8)
	s_waitcnt lgkmcnt(0)
	s_barrier
	ds_read_b128 v[34:37], v131
	ds_read_b128 v[38:41], v131 offset:2048
	ds_read_b128 v[74:77], v131 offset:4096
	ds_read_b128 v[78:81], v131 offset:6144
	ds_read_b128 v[82:85], v129
	ds_read_b128 v[86:89], v129 offset:2048
	s_add_u32 s70, s22, 0x300
	v_add_u32_e32 v95, 0x8000, v94
	v_lshl_add_u64 v[0:1], s[26:27], 0, v[196:197]
	s_addc_u32 s71, s90, 0
	v_readfirstlane_b32 s0, v95
	s_mov_b32 m0, s0
	v_cvt_pk_f16_f32 v33, v32, v33
	global_load_lds_dwordx4 v[0:1], off
	v_cvt_pk_f16_f32 v32, v30, v31
	ds_write_b64 v100, v[32:33] offset:32768
	s_setprio 1
	s_waitcnt lgkmcnt(1)
	v_mfma_f32_16x16x32_f16 v[90:93], v[82:85], v[34:37], 0
	v_mfma_f32_16x16x32_f16 v[102:105], v[82:85], v[38:41], 0
	v_mfma_f32_16x16x32_f16 v[106:109], v[82:85], v[74:77], 0
	v_mfma_f32_16x16x32_f16 v[82:85], v[82:85], v[78:81], 0
	v_mfma_f32_16x16x32_f16 v[110:113], v[86:89], v[34:37], 0
	v_mfma_f32_16x16x32_f16 v[114:117], v[86:89], v[38:41], 0
	v_mfma_f32_16x16x32_f16 v[118:121], v[86:89], v[74:77], 0
	v_mfma_f32_16x16x32_f16 v[86:89], v[86:89], v[78:81], 0
	s_setprio 0
	ds_read_b128 v[122:125], v129 offset:4096
	ds_read_b128 v[134:137], v129 offset:6144
	v_add_u32_e32 v96, 0xa000, v94
	v_lshl_add_u64 v[98:99], v[0:1], 0, s[58:59]
	v_readfirstlane_b32 s1, v96
	s_mov_b32 m0, s1
	v_cvt_pk_f16_f32 v29, v28, v29
	global_load_lds_dwordx4 v[98:99], off
	v_cvt_pk_f16_f32 v28, v26, v27
	ds_write_b64 v100, v[28:29] offset:36864
	s_add_u32 s70, s22, 0x20300
	s_addc_u32 s71, s90, 0
	s_add_u32 s100, s22, 0x300
	s_addc_u32 s101, s90, 0
	global_load_dwordx4 v[30:33], v201, s[100:101] nt
	s_setprio 1
	s_waitcnt lgkmcnt(1)
	v_mfma_f32_16x16x32_f16 v[138:141], v[122:125], v[34:37], 0
	v_mfma_f32_16x16x32_f16 v[142:145], v[122:125], v[38:41], 0
	v_mfma_f32_16x16x32_f16 v[146:149], v[122:125], v[74:77], 0
	v_mfma_f32_16x16x32_f16 v[122:125], v[122:125], v[78:81], 0
	v_mfma_f32_16x16x32_f16 v[150:153], v[134:137], v[34:37], 0
	v_mfma_f32_16x16x32_f16 v[154:157], v[134:137], v[38:41], 0
	v_mfma_f32_16x16x32_f16 v[158:161], v[134:137], v[74:77], 0
	v_mfma_f32_16x16x32_f16 v[134:137], v[134:137], v[78:81], 0
	s_setprio 0
	ds_read_b128 v[162:165], v129 offset:8192
	ds_read_b128 v[166:169], v129 offset:10240
	v_add_u32_e32 v97, 0xc000, v94
	v_lshl_add_u64 v[98:99], v[0:1], 0, s[60:61]
	v_readfirstlane_b32 s71, v97
	s_mov_b32 m0, s71
	v_cvt_pk_f16_f32 v25, v24, v25
	global_load_lds_dwordx4 v[98:99], off
	v_cvt_pk_f16_f32 v24, v22, v23
	ds_write_b64 v100, v[24:25] offset:40960
	s_add_u32 s72, s22, 0x40300
	s_addc_u32 s73, s90, 0
	s_add_u32 s100, s22, 0x20300
	s_addc_u32 s101, s90, 0
	global_load_dwordx4 v[26:29], v201, s[100:101] nt
	s_setprio 1
	s_waitcnt lgkmcnt(1)
	v_mfma_f32_16x16x32_f16 v[170:173], v[162:165], v[34:37], 0
	v_mfma_f32_16x16x32_f16 v[174:177], v[162:165], v[38:41], 0
	v_mfma_f32_16x16x32_f16 v[178:181], v[162:165], v[74:77], 0
	v_mfma_f32_16x16x32_f16 v[162:165], v[162:165], v[78:81], 0
	v_mfma_f32_16x16x32_f16 v[182:185], v[166:169], v[34:37], 0
	v_mfma_f32_16x16x32_f16 v[186:189], v[166:169], v[38:41], 0
	v_mfma_f32_16x16x32_f16 v[190:193], v[166:169], v[74:77], 0
	v_mfma_f32_16x16x32_f16 v[166:169], v[166:169], v[78:81], 0
	s_setprio 0
	ds_read_b128 v[202:205], v129 offset:12288
	ds_read_b128 v[206:209], v129 offset:14336
	v_add_u32_e32 v98, 0xe000, v94
	v_lshl_add_u64 v[0:1], v[0:1], 0, s[62:63]
	v_readfirstlane_b32 s72, v98
	s_mov_b32 m0, s72
	s_nop 0
	global_load_lds_dwordx4 v[0:1], off
	v_cvt_pk_f16_f32 v1, v20, v21
	v_cvt_pk_f16_f32 v0, v18, v19
	ds_write_b64 v100, v[0:1] offset:45056
	s_add_u32 s80, s22, 0x60300
	s_addc_u32 s81, s90, 0
	s_add_u32 s100, s22, 0x40300
	s_addc_u32 s101, s90, 0
	global_load_dwordx4 v[22:25], v201, s[100:101] nt
	s_setprio 1
	s_waitcnt lgkmcnt(1)
	v_mfma_f32_16x16x32_f16 v[210:213], v[202:205], v[34:37], 0
	v_mfma_f32_16x16x32_f16 v[214:217], v[202:205], v[38:41], 0
	v_mfma_f32_16x16x32_f16 v[218:221], v[202:205], v[74:77], 0
	v_mfma_f32_16x16x32_f16 v[202:205], v[202:205], v[78:81], 0
	v_mfma_f32_16x16x32_f16 v[74:77], v[206:209], v[74:77], 0
	v_mfma_f32_16x16x32_f16 v[78:81], v[206:209], v[78:81], 0
	v_mfma_f32_16x16x32_f16 v[222:225], v[206:209], v[34:37], 0
	v_mfma_f32_16x16x32_f16 v[226:229], v[206:209], v[38:41], 0
	s_setprio 0
	ds_read_b128 v[206:209], v128
	ds_read_b128 v[230:233], v128 offset:2048
	ds_read_b128 v[234:237], v128 offset:4096
	ds_read_b128 v[238:241], v128 offset:6144
	ds_read_b128 v[34:37], v130
	ds_read_b128 v[38:41], v130 offset:2048
	v_cvt_pk_f16_f32 v1, v16, v17
	v_cvt_pk_f16_f32 v0, v14, v15
	ds_write_b64 v100, v[0:1] offset:49152
	s_add_u32 s80, s22, 0x80300
	s_addc_u32 s81, s90, 0
	s_add_u32 s100, s22, 0x60300
	s_addc_u32 s101, s90, 0
	global_load_dwordx4 v[18:21], v201, s[100:101] nt
	s_setprio 1
	s_waitcnt lgkmcnt(1)
	v_mfma_f32_16x16x32_f16 v[90:93], v[34:37], v[206:209], v[90:93]
	v_mfma_f32_16x16x32_f16 v[102:105], v[34:37], v[230:233], v[102:105]
	v_mfma_f32_16x16x32_f16 v[106:109], v[34:37], v[234:237], v[106:109]
	v_mfma_f32_16x16x32_f16 v[82:85], v[34:37], v[238:241], v[82:85]
	v_mfma_f32_16x16x32_f16 v[110:113], v[38:41], v[206:209], v[110:113]
	v_mfma_f32_16x16x32_f16 v[114:117], v[38:41], v[230:233], v[114:117]
	v_mfma_f32_16x16x32_f16 v[118:121], v[38:41], v[234:237], v[118:121]
	v_mfma_f32_16x16x32_f16 v[86:89], v[38:41], v[238:241], v[86:89]
	s_setprio 0
	ds_read_b128 v[34:37], v130 offset:4096
	ds_read_b128 v[38:41], v130 offset:6144
	v_cvt_pk_f16_f32 v1, v12, v13
	v_cvt_pk_f16_f32 v0, v10, v11
	ds_write_b64 v100, v[0:1] offset:53248
	s_add_u32 s80, s22, 0xa0300
	s_addc_u32 s81, s90, 0
	s_add_u32 s100, s22, 0x80300
	s_addc_u32 s101, s90, 0
	global_load_dwordx4 v[14:17], v201, s[100:101] nt
	s_setprio 1
	s_waitcnt lgkmcnt(1)
	v_mfma_f32_16x16x32_f16 v[146:149], v[34:37], v[234:237], v[146:149]
	v_mfma_f32_16x16x32_f16 v[122:125], v[34:37], v[238:241], v[122:125]
	v_mfma_f32_16x16x32_f16 v[134:137], v[38:41], v[238:241], v[134:137]
	v_mfma_f32_16x16x32_f16 v[138:141], v[34:37], v[206:209], v[138:141]
	v_mfma_f32_16x16x32_f16 v[142:145], v[34:37], v[230:233], v[142:145]
	v_mfma_f32_16x16x32_f16 v[150:153], v[38:41], v[206:209], v[150:153]
	v_mfma_f32_16x16x32_f16 v[154:157], v[38:41], v[230:233], v[154:157]
	v_mfma_f32_16x16x32_f16 v[158:161], v[38:41], v[234:237], v[158:161]
	s_setprio 0
	ds_read_b128 v[38:41], v130 offset:8192
	ds_read_b128 v[242:245], v130 offset:10240
	v_cvt_pk_f16_f32 v1, v8, v9
	v_cvt_pk_f16_f32 v0, v6, v7
	ds_write_b64 v100, v[0:1] offset:57344
	s_add_u32 s80, s22, 0xc0300
	s_addc_u32 s81, s90, 0
	s_add_u32 s100, s22, 0xa0300
	s_addc_u32 s101, s90, 0
	global_load_dwordx4 v[10:13], v201, s[100:101] nt
	s_add_u32 s100, s22, 0xc0300
	s_addc_u32 s101, s90, 0
	global_load_dwordx4 v[34:37], v201, s[100:101] nt
	s_setprio 1
	s_waitcnt lgkmcnt(1)
	v_mfma_f32_16x16x32_f16 v[6:9], v[38:41], v[206:209], v[170:173]
	v_mfma_f32_16x16x32_f16 v[170:173], v[38:41], v[230:233], v[174:177]
	v_mfma_f32_16x16x32_f16 v[174:177], v[38:41], v[234:237], v[178:181]
	v_mfma_f32_16x16x32_f16 v[162:165], v[38:41], v[238:241], v[162:165]
	v_mfma_f32_16x16x32_f16 v[178:181], v[242:245], v[206:209], v[182:185]
	v_mfma_f32_16x16x32_f16 v[182:185], v[242:245], v[230:233], v[186:189]
	v_mfma_f32_16x16x32_f16 v[186:189], v[242:245], v[234:237], v[190:193]
	v_mfma_f32_16x16x32_f16 v[166:169], v[242:245], v[238:241], v[166:169]
	s_setprio 0
	s_nop 0
	ds_read_b128 v[190:193], v130 offset:12288
	ds_read_b128 v[242:245], v130 offset:14336
	v_cvt_pk_f16_f32 v1, v4, v5
	v_cvt_pk_f16_f32 v0, v2, v3
	ds_write_b64 v100, v[0:1] offset:61440
	s_add_u32 s80, s22, 0xe0300
	s_addc_u32 s81, s90, 0
	s_add_u32 s100, s22, 0xe0300
	s_addc_u32 s101, s90, 0
	global_load_dwordx4 v[38:41], v201, s[100:101] nt
	s_setprio 1
	s_waitcnt lgkmcnt(1)
	v_mfma_f32_16x16x32_f16 v[78:81], v[242:245], v[238:241], v[78:81]
	v_mfma_f32_16x16x32_f16 v[210:213], v[190:193], v[206:209], v[210:213]
	v_mfma_f32_16x16x32_f16 v[214:217], v[190:193], v[230:233], v[214:217]
	v_mfma_f32_16x16x32_f16 v[218:221], v[190:193], v[234:237], v[218:221]
	v_mfma_f32_16x16x32_f16 v[190:193], v[190:193], v[238:241], v[202:205]
	v_mfma_f32_16x16x32_f16 v[202:205], v[242:245], v[206:209], v[222:225]
	v_mfma_f32_16x16x32_f16 v[206:209], v[242:245], v[230:233], v[226:229]
	v_mfma_f32_16x16x32_f16 v[222:225], v[242:245], v[234:237], v[74:77]
	s_setprio 0
	s_waitcnt vmcnt(6)
	s_waitcnt lgkmcnt(0)
	s_barrier
	ds_read_b128 v[226:229], v131 offset:32768
	ds_read_b128 v[230:233], v131 offset:34816
	ds_read_b128 v[234:237], v131 offset:36864
	ds_read_b128 v[238:241], v131 offset:38912
	ds_read_b128 v[74:77], v129 offset:32768
	ds_read_b128 v[242:245], v129 offset:34816
	s_add_u32 s80, s22, 0x400
	s_addc_u32 s81, s90, 0
	v_lshl_add_u64 v[198:199], s[28:29], 0, v[196:197]
	v_readfirstlane_b32 s70, v94
	s_mov_b32 m0, s70
	v_cvt_pk_f16_f32 v1, v72, v73
	global_load_lds_dwordx4 v[198:199], off
	v_cvt_pk_f16_f32 v0, v70, v71
	ds_write_b64 v100, v[0:1]
	s_setprio 1
	s_waitcnt lgkmcnt(1)
	v_mfma_f32_16x16x32_f16 v[70:73], v[74:77], v[226:229], v[90:93]
	v_mfma_f32_16x16x32_f16 v[90:93], v[74:77], v[230:233], v[102:105]
	v_mfma_f32_16x16x32_f16 v[104:107], v[74:77], v[234:237], v[106:109]
	v_mfma_f32_16x16x32_f16 v[82:85], v[74:77], v[238:241], v[82:85]
	v_mfma_f32_16x16x32_f16 v[108:111], v[242:245], v[226:229], v[110:113]
	v_mfma_f32_16x16x32_f16 v[112:115], v[242:245], v[230:233], v[114:117]
	v_mfma_f32_16x16x32_f16 v[116:119], v[242:245], v[234:237], v[118:121]
	v_mfma_f32_16x16x32_f16 v[86:89], v[242:245], v[238:241], v[86:89]
	s_setprio 0
	ds_read_b128 v[74:77], v129 offset:36864
	ds_read_b128 v[242:245], v129 offset:38912
	v_add_u32_e32 v99, 0x2000, v94
	v_lshl_add_u64 v[4:5], v[198:199], 0, s[58:59]
	v_readfirstlane_b32 s73, v99
	s_mov_b32 m0, s73
	s_nop 0
	global_load_lds_dwordx4 v[4:5], off
	v_cvt_pk_f16_f32 v5, v44, v45
	v_cvt_pk_f16_f32 v4, v42, v43
	ds_write_b64 v100, v[4:5] offset:4096
	s_add_u32 s80, s22, 0x20400
	s_addc_u32 s81, s90, 0
	s_add_u32 s100, s22, 0x400
	s_addc_u32 s101, s90, 0
	global_load_dwordx4 v[0:3], v201, s[100:101] nt
	s_setprio 1
	s_waitcnt lgkmcnt(1)
	v_mfma_f32_16x16x32_f16 v[146:149], v[74:77], v[234:237], v[146:149]
	v_mfma_f32_16x16x32_f16 v[120:123], v[74:77], v[238:241], v[122:125]
	v_mfma_f32_16x16x32_f16 v[124:127], v[242:245], v[226:229], v[150:153]
	v_mfma_f32_16x16x32_f16 v[134:137], v[242:245], v[238:241], v[134:137]
	v_mfma_f32_16x16x32_f16 v[138:141], v[74:77], v[226:229], v[138:141]
	v_mfma_f32_16x16x32_f16 v[142:145], v[74:77], v[230:233], v[142:145]
	v_mfma_f32_16x16x32_f16 v[150:153], v[242:245], v[230:233], v[154:157]
	v_mfma_f32_16x16x32_f16 v[154:157], v[242:245], v[234:237], v[158:161]
	s_setprio 0
	ds_read_b128 v[74:77], v129 offset:40960
	s_nop 0
	ds_read_b128 v[158:161], v129 offset:43008
	v_add_u32_e32 v101, 0x4000, v94
	v_lshl_add_u64 v[4:5], v[198:199], 0, s[60:61]
	v_readfirstlane_b32 s91, v101
	s_mov_b32 m0, s91
	s_nop 0
	global_load_lds_dwordx4 v[4:5], off
	v_cvt_pk_f16_f32 v5, v48, v49
	v_cvt_pk_f16_f32 v4, v46, v47
	ds_write_b64 v100, v[4:5] offset:8192
	s_add_u32 s80, s22, 0x40400
	s_addc_u32 s81, s90, 0
	s_add_u32 s100, s22, 0x20400
	s_addc_u32 s101, s90, 0
	global_load_dwordx4 v[42:45], v201, s[100:101] nt
	s_setprio 1
	s_waitcnt lgkmcnt(1)
	v_mfma_f32_16x16x32_f16 v[4:7], v[74:77], v[226:229], v[6:9]
	v_mfma_f32_16x16x32_f16 v[170:173], v[74:77], v[230:233], v[170:173]
	v_mfma_f32_16x16x32_f16 v[174:177], v[74:77], v[234:237], v[174:177]
	v_mfma_f32_16x16x32_f16 v[162:165], v[74:77], v[238:241], v[162:165]
	v_mfma_f32_16x16x32_f16 v[178:181], v[158:161], v[226:229], v[178:181]
	v_mfma_f32_16x16x32_f16 v[182:185], v[158:161], v[230:233], v[182:185]
	v_mfma_f32_16x16x32_f16 v[186:189], v[158:161], v[234:237], v[186:189]
	v_mfma_f32_16x16x32_f16 v[158:161], v[158:161], v[238:241], v[166:169]
	s_setprio 0
	s_nop 1
	ds_read_b128 v[166:169], v129 offset:45056
	ds_read_b128 v[242:245], v129 offset:47104
	v_add_u32_e32 v102, 0x6000, v94
	v_lshl_add_u64 v[8:9], v[198:199], 0, s[62:63]
	v_readfirstlane_b32 s92, v102
	s_mov_b32 m0, s92
	s_nop 0
	global_load_lds_dwordx4 v[8:9], off
	v_cvt_pk_f16_f32 v9, v68, v69
	v_cvt_pk_f16_f32 v8, v66, v67
	ds_write_b64 v100, v[8:9] offset:12288
	s_add_u32 s80, s22, 0x60400
	s_addc_u32 s81, s90, 0
	s_add_u32 s100, s22, 0x40400
	s_addc_u32 s101, s90, 0
	global_load_dwordx4 v[46:49], v201, s[100:101] nt
	s_setprio 1
	s_waitcnt lgkmcnt(1)
	v_mfma_f32_16x16x32_f16 v[66:69], v[166:169], v[226:229], v[210:213]
	v_mfma_f32_16x16x32_f16 v[210:213], v[166:169], v[230:233], v[214:217]
	v_mfma_f32_16x16x32_f16 v[214:217], v[166:169], v[234:237], v[218:221]
	v_mfma_f32_16x16x32_f16 v[166:169], v[166:169], v[238:241], v[190:193]
	v_mfma_f32_16x16x32_f16 v[190:193], v[242:245], v[226:229], v[202:205]
	v_mfma_f32_16x16x32_f16 v[202:205], v[242:245], v[230:233], v[206:209]
	v_mfma_f32_16x16x32_f16 v[206:209], v[242:245], v[234:237], v[222:225]
	v_mfma_f32_16x16x32_f16 v[218:221], v[242:245], v[238:241], v[78:81]
	s_setprio 0
	s_nop 0
	ds_read_b128 v[222:225], v128 offset:32768
	ds_read_b128 v[226:229], v128 offset:34816
	ds_read_b128 v[230:233], v128 offset:36864
	ds_read_b128 v[234:237], v128 offset:38912
	ds_read_b128 v[238:241], v130 offset:32768
	ds_read_b128 v[242:245], v130 offset:34816
	v_cvt_pk_f16_f32 v9, v64, v65
	v_cvt_pk_f16_f32 v8, v62, v63
	ds_write_b64 v100, v[8:9] offset:16384
	s_add_u32 s80, s22, 0x80400
	s_addc_u32 s81, s90, 0
	s_add_u32 s100, s22, 0x60400
	s_addc_u32 s101, s90, 0
	global_load_dwordx4 v[74:77], v201, s[100:101] nt
	s_setprio 1
	s_waitcnt lgkmcnt(1)
	v_mfma_f32_16x16x32_f16 v[62:65], v[238:241], v[222:225], v[70:73]
	v_mfma_f32_16x16x32_f16 v[70:73], v[238:241], v[226:229], v[90:93]
	v_mfma_f32_16x16x32_f16 v[104:107], v[238:241], v[230:233], v[104:107]
	v_mfma_f32_16x16x32_f16 v[108:111], v[242:245], v[222:225], v[108:111]
	v_mfma_f32_16x16x32_f16 v[112:115], v[242:245], v[226:229], v[112:115]
	v_mfma_f32_16x16x32_f16 v[116:119], v[242:245], v[230:233], v[116:119]
	v_mfma_f32_16x16x32_f16 v[238:241], v[238:241], v[234:237], v[82:85]
	v_mfma_f32_16x16x32_f16 v[242:245], v[242:245], v[234:237], v[86:89]
	s_setprio 0
	s_nop 1
	ds_read_b128 v[86:89], v130 offset:36864
	ds_read_b128 v[90:93], v130 offset:38912
	v_cvt_pk_f16_f32 v9, v60, v61
	v_cvt_pk_f16_f32 v8, v58, v59
	ds_write_b64 v100, v[8:9] offset:20480
	s_add_u32 s80, s22, 0xa0400
	s_addc_u32 s81, s90, 0
	s_add_u32 s100, s22, 0x80400
	s_addc_u32 s101, s90, 0
	global_load_dwordx4 v[78:81], v201, s[100:101] nt
	s_setprio 1
	s_waitcnt lgkmcnt(1)
	v_mfma_f32_16x16x32_f16 v[58:61], v[86:89], v[222:225], v[138:141]
	v_mfma_f32_16x16x32_f16 v[138:141], v[86:89], v[226:229], v[142:145]
	v_mfma_f32_16x16x32_f16 v[142:145], v[86:89], v[230:233], v[146:149]
	v_mfma_f32_16x16x32_f16 v[120:123], v[86:89], v[234:237], v[120:123]
	v_mfma_f32_16x16x32_f16 v[124:127], v[90:93], v[222:225], v[124:127]
	v_mfma_f32_16x16x32_f16 v[146:149], v[90:93], v[226:229], v[150:153]
	v_mfma_f32_16x16x32_f16 v[134:137], v[90:93], v[234:237], v[134:137]
	v_mfma_f32_16x16x32_f16 v[150:153], v[90:93], v[230:233], v[154:157]
	s_setprio 0
	ds_read_b128 v[90:93], v130 offset:40960
	s_nop 0
	ds_read_b128 v[154:157], v130 offset:43008
	v_cvt_pk_f16_f32 v9, v56, v57
	v_cvt_pk_f16_f32 v8, v54, v55
	ds_write_b64 v100, v[8:9] offset:24576
	s_add_u32 s80, s22, 0xc0400
	s_addc_u32 s81, s90, 0
	s_add_u32 s100, s22, 0xa0400
	s_addc_u32 s101, s90, 0
	global_load_dwordx4 v[82:85], v201, s[100:101] nt
	s_add_u32 s100, s22, 0xc0400
	s_addc_u32 s101, s90, 0
	global_load_dwordx4 v[86:89], v201, s[100:101] nt
	s_setprio 1
	s_waitcnt lgkmcnt(1)
	v_mfma_f32_16x16x32_f16 v[246:249], v[90:93], v[222:225], v[4:7]
	v_mfma_f32_16x16x32_f16 v[170:173], v[90:93], v[226:229], v[170:173]
	v_mfma_f32_16x16x32_f16 v[174:177], v[90:93], v[230:233], v[174:177]
	v_mfma_f32_16x16x32_f16 v[162:165], v[90:93], v[234:237], v[162:165]
	v_mfma_f32_16x16x32_f16 v[178:181], v[154:157], v[222:225], v[178:181]
	v_mfma_f32_16x16x32_f16 v[182:185], v[154:157], v[226:229], v[182:185]
	v_mfma_f32_16x16x32_f16 v[186:189], v[154:157], v[230:233], v[186:189]
	v_mfma_f32_16x16x32_f16 v[154:157], v[154:157], v[234:237], v[158:161]
	s_setprio 0
	ds_read_b128 v[4:7], v130 offset:45056
	ds_read_b128 v[54:57], v130 offset:47104
	v_cvt_pk_f16_f32 v9, v52, v53
	v_cvt_pk_f16_f32 v8, v50, v51
	ds_write_b64 v100, v[8:9] offset:28672
	s_add_u32 s80, s22, 0xe0400
	s_addc_u32 s81, s90, 0
	s_add_u32 s100, s22, 0xe0400
	s_addc_u32 s101, s90, 0
	global_load_dwordx4 v[90:93], v201, s[100:101] nt
	s_setprio 1
	s_waitcnt lgkmcnt(1)
	v_mfma_f32_16x16x32_f16 v[66:69], v[4:7], v[222:225], v[66:69]
	v_mfma_f32_16x16x32_f16 v[158:161], v[4:7], v[226:229], v[210:213]
	v_mfma_f32_16x16x32_f16 v[210:213], v[4:7], v[230:233], v[214:217]
	v_mfma_f32_16x16x32_f16 v[166:169], v[4:7], v[234:237], v[166:169]
	v_mfma_f32_16x16x32_f16 v[190:193], v[54:57], v[222:225], v[190:193]
	v_mfma_f32_16x16x32_f16 v[202:205], v[54:57], v[226:229], v[202:205]
	v_mfma_f32_16x16x32_f16 v[206:209], v[54:57], v[230:233], v[206:209]
	v_mfma_f32_16x16x32_f16 v[214:217], v[54:57], v[234:237], v[218:221]
	s_setprio 0
	s_waitcnt vmcnt(6)
	s_waitcnt lgkmcnt(0)
	s_barrier
	s_nop 0
	ds_read_b128 v[218:221], v131
	ds_read_b128 v[222:225], v131 offset:2048
	ds_read_b128 v[226:229], v131 offset:4096
	ds_read_b128 v[230:233], v131 offset:6144
	ds_read_b128 v[50:53], v129
	ds_read_b128 v[54:57], v129 offset:2048
	s_add_u32 s80, s22, 0x500
	v_lshl_add_u64 v[8:9], s[30:31], 0, v[196:197]
	s_addc_u32 s81, s90, 0
	s_mov_b32 m0, s0
	v_cvt_pk_f16_f32 v5, v32, v33
	global_load_lds_dwordx4 v[8:9], off
	v_cvt_pk_f16_f32 v4, v30, v31
	ds_write_b64 v100, v[4:5] offset:32768
	s_setprio 1
	s_waitcnt lgkmcnt(1)
	v_mfma_f32_16x16x32_f16 v[30:33], v[50:53], v[218:221], v[62:65]
	v_mfma_f32_16x16x32_f16 v[70:73], v[50:53], v[222:225], v[70:73]
	v_mfma_f32_16x16x32_f16 v[104:107], v[50:53], v[226:229], v[104:107]
	v_mfma_f32_16x16x32_f16 v[108:111], v[54:57], v[218:221], v[108:111]
	v_mfma_f32_16x16x32_f16 v[112:115], v[54:57], v[222:225], v[112:115]
	v_mfma_f32_16x16x32_f16 v[116:119], v[54:57], v[226:229], v[116:119]
	v_mfma_f32_16x16x32_f16 v[234:237], v[50:53], v[230:233], v[238:241]
	v_mfma_f32_16x16x32_f16 v[238:241], v[54:57], v[230:233], v[242:245]
	s_setprio 0
	ds_read_b128 v[54:57], v129 offset:4096
	ds_read_b128 v[62:65], v129 offset:6144
	s_mov_b32 m0, s1
	v_lshl_add_u64 v[50:51], v[8:9], 0, s[58:59]
	global_load_lds_dwordx4 v[50:51], off
	v_cvt_pk_f16_f32 v29, v28, v29
	v_cvt_pk_f16_f32 v28, v26, v27
	ds_write_b64 v100, v[28:29] offset:36864
	s_add_u32 s0, s22, 0x20500
	s_addc_u32 s1, s90, 0
	s_add_u32 s100, s22, 0x500
	s_addc_u32 s101, s90, 0
	global_load_dwordx4 v[4:7], v201, s[100:101] nt
	s_setprio 1
	s_waitcnt lgkmcnt(1)
	v_mfma_f32_16x16x32_f16 v[26:29], v[54:57], v[218:221], v[58:61]
	v_mfma_f32_16x16x32_f16 v[120:123], v[54:57], v[230:233], v[120:123]
	v_mfma_f32_16x16x32_f16 v[124:127], v[62:65], v[218:221], v[124:127]
	v_mfma_f32_16x16x32_f16 v[146:149], v[62:65], v[222:225], v[146:149]
	v_mfma_f32_16x16x32_f16 v[134:137], v[62:65], v[230:233], v[134:137]
	v_mfma_f32_16x16x32_f16 v[138:141], v[54:57], v[222:225], v[138:141]
	v_mfma_f32_16x16x32_f16 v[142:145], v[54:57], v[226:229], v[142:145]
	v_mfma_f32_16x16x32_f16 v[150:153], v[62:65], v[226:229], v[150:153]
	s_setprio 0
	ds_read_b128 v[58:61], v129 offset:8192
	ds_read_b128 v[62:65], v129 offset:10240
	s_mov_b32 m0, s71
	v_lshl_add_u64 v[54:55], v[8:9], 0, s[60:61]
	global_load_lds_dwordx4 v[54:55], off
	v_cvt_pk_f16_f32 v25, v24, v25
	v_cvt_pk_f16_f32 v24, v22, v23
	ds_write_b64 v100, v[24:25] offset:40960
	s_add_u32 s0, s22, 0x40500
	s_addc_u32 s1, s90, 0
	s_add_u32 s100, s22, 0x20500
	s_addc_u32 s101, s90, 0
	global_load_dwordx4 v[50:53], v201, s[100:101] nt
	s_setprio 1
	s_waitcnt lgkmcnt(1)
	v_mfma_f32_16x16x32_f16 v[22:25], v[58:61], v[218:221], v[246:249]
	v_mfma_f32_16x16x32_f16 v[170:173], v[58:61], v[222:225], v[170:173]
	v_mfma_f32_16x16x32_f16 v[174:177], v[58:61], v[226:229], v[174:177]
	v_mfma_f32_16x16x32_f16 v[162:165], v[58:61], v[230:233], v[162:165]
	v_mfma_f32_16x16x32_f16 v[178:181], v[62:65], v[218:221], v[178:181]
	v_mfma_f32_16x16x32_f16 v[182:185], v[62:65], v[222:225], v[182:185]
	v_mfma_f32_16x16x32_f16 v[186:189], v[62:65], v[226:229], v[186:189]
	v_mfma_f32_16x16x32_f16 v[154:157], v[62:65], v[230:233], v[154:157]
	s_setprio 0
	ds_read_b128 v[62:65], v129 offset:12288
	ds_read_b128 v[242:245], v129 offset:14336
	s_mov_b32 m0, s72
	v_lshl_add_u64 v[8:9], v[8:9], 0, s[62:63]
	global_load_lds_dwordx4 v[8:9], off
	v_cvt_pk_f16_f32 v9, v20, v21
	v_cvt_pk_f16_f32 v8, v18, v19
	ds_write_b64 v100, v[8:9] offset:45056
	s_add_u32 s0, s22, 0x60500
	s_addc_u32 s1, s90, 0
	s_add_u32 s100, s22, 0x40500
	s_addc_u32 s101, s90, 0
	global_load_dwordx4 v[54:57], v201, s[100:101] nt
	s_setprio 1
	s_waitcnt lgkmcnt(1)
	v_mfma_f32_16x16x32_f16 v[18:21], v[62:65], v[218:221], v[66:69]
	v_mfma_f32_16x16x32_f16 v[158:161], v[62:65], v[222:225], v[158:161]
	v_mfma_f32_16x16x32_f16 v[210:213], v[62:65], v[226:229], v[210:213]
	v_mfma_f32_16x16x32_f16 v[166:169], v[62:65], v[230:233], v[166:169]
	v_mfma_f32_16x16x32_f16 v[190:193], v[242:245], v[218:221], v[190:193]
	v_mfma_f32_16x16x32_f16 v[202:205], v[242:245], v[222:225], v[202:205]
	v_mfma_f32_16x16x32_f16 v[206:209], v[242:245], v[226:229], v[206:209]
	v_mfma_f32_16x16x32_f16 v[214:217], v[242:245], v[230:233], v[214:217]
	s_setprio 0
	ds_read_b128 v[218:221], v128
	ds_read_b128 v[222:225], v128 offset:2048
	ds_read_b128 v[226:229], v128 offset:4096
	ds_read_b128 v[230:233], v128 offset:6144
	ds_read_b128 v[66:69], v130
	ds_read_b128 v[242:245], v130 offset:2048
	v_cvt_pk_f16_f32 v9, v16, v17
	v_cvt_pk_f16_f32 v8, v14, v15
	ds_write_b64 v100, v[8:9] offset:49152
	s_add_u32 s0, s22, 0x80500
	s_addc_u32 s1, s90, 0
	s_add_u32 s100, s22, 0x60500
	s_addc_u32 s101, s90, 0
	global_load_dwordx4 v[58:61], v201, s[100:101] nt
	s_setprio 1
	s_waitcnt lgkmcnt(1)
	v_mfma_f32_16x16x32_f16 v[14:17], v[66:69], v[218:221], v[30:33]
	v_mfma_f32_16x16x32_f16 v[30:33], v[66:69], v[222:225], v[70:73]
	v_mfma_f32_16x16x32_f16 v[104:107], v[66:69], v[226:229], v[104:107]
	v_mfma_f32_16x16x32_f16 v[108:111], v[242:245], v[218:221], v[108:111]
	v_mfma_f32_16x16x32_f16 v[112:115], v[242:245], v[222:225], v[112:115]
	v_mfma_f32_16x16x32_f16 v[116:119], v[242:245], v[226:229], v[116:119]
	v_mfma_f32_16x16x32_f16 v[234:237], v[66:69], v[230:233], v[234:237]
	v_mfma_f32_16x16x32_f16 v[238:241], v[242:245], v[230:233], v[238:241]
	s_setprio 0
	ds_read_b128 v[70:73], v130 offset:4096
	ds_read_b128 v[242:245], v130 offset:6144
	v_cvt_pk_f16_f32 v9, v12, v13
	v_cvt_pk_f16_f32 v8, v10, v11
	ds_write_b64 v100, v[8:9] offset:53248
	s_add_u32 s0, s22, 0xa0500
	s_addc_u32 s1, s90, 0
	s_add_u32 s100, s22, 0x80500
	s_addc_u32 s101, s90, 0
	global_load_dwordx4 v[62:65], v201, s[100:101] nt
	s_setprio 1
	s_waitcnt lgkmcnt(1)
	v_mfma_f32_16x16x32_f16 v[26:29], v[70:73], v[218:221], v[26:29]
	v_mfma_f32_16x16x32_f16 v[120:123], v[70:73], v[230:233], v[120:123]
	v_mfma_f32_16x16x32_f16 v[124:127], v[242:245], v[218:221], v[124:127]
	v_mfma_f32_16x16x32_f16 v[146:149], v[242:245], v[222:225], v[146:149]
	v_mfma_f32_16x16x32_f16 v[134:137], v[242:245], v[230:233], v[134:137]
	v_mfma_f32_16x16x32_f16 v[138:141], v[70:73], v[222:225], v[138:141]
	v_mfma_f32_16x16x32_f16 v[142:145], v[70:73], v[226:229], v[142:145]
	v_mfma_f32_16x16x32_f16 v[150:153], v[242:245], v[226:229], v[150:153]
	s_setprio 0
	ds_read_b128 v[8:11], v130 offset:8192
	ds_read_b128 v[242:245], v130 offset:10240
	v_cvt_pk_f16_f32 v13, v36, v37
	v_cvt_pk_f16_f32 v12, v34, v35
	ds_write_b64 v100, v[12:13] offset:57344
	s_add_u32 s0, s22, 0xc0500
	s_addc_u32 s1, s90, 0
	s_add_u32 s100, s22, 0xa0500
	s_addc_u32 s101, s90, 0
	global_load_dwordx4 v[66:69], v201, s[100:101] nt
	s_add_u32 s100, s22, 0xc0500
	s_addc_u32 s101, s90, 0
	global_load_dwordx4 v[70:73], v201, s[100:101] nt
	s_setprio 1
	s_waitcnt lgkmcnt(1)
	v_mfma_f32_16x16x32_f16 v[22:25], v[8:11], v[218:221], v[22:25]
	v_mfma_f32_16x16x32_f16 v[170:173], v[8:11], v[222:225], v[170:173]
	v_mfma_f32_16x16x32_f16 v[174:177], v[8:11], v[226:229], v[174:177]
	v_mfma_f32_16x16x32_f16 v[162:165], v[8:11], v[230:233], v[162:165]
	v_mfma_f32_16x16x32_f16 v[178:181], v[242:245], v[218:221], v[178:181]
	v_mfma_f32_16x16x32_f16 v[182:185], v[242:245], v[222:225], v[182:185]
	v_mfma_f32_16x16x32_f16 v[186:189], v[242:245], v[226:229], v[186:189]
	v_mfma_f32_16x16x32_f16 v[154:157], v[242:245], v[230:233], v[154:157]
	s_setprio 0
	ds_read_b128 v[8:11], v130 offset:12288
	ds_read_b128 v[242:245], v130 offset:14336
	v_cvt_pk_f16_f32 v13, v40, v41
	v_cvt_pk_f16_f32 v12, v38, v39
	ds_write_b64 v100, v[12:13] offset:61440
	s_add_u32 s0, s22, 0xe0500
	s_addc_u32 s1, s90, 0
	s_add_u32 s100, s22, 0xe0500
	s_addc_u32 s101, s90, 0
	global_load_dwordx4 v[36:39], v201, s[100:101] nt
	s_setprio 1
	s_waitcnt lgkmcnt(1)
	v_mfma_f32_16x16x32_f16 v[246:249], v[8:11], v[218:221], v[18:21]
	v_mfma_f32_16x16x32_f16 v[158:161], v[8:11], v[222:225], v[158:161]
	v_mfma_f32_16x16x32_f16 v[210:213], v[8:11], v[226:229], v[210:213]
	v_mfma_f32_16x16x32_f16 v[166:169], v[8:11], v[230:233], v[166:169]
	v_mfma_f32_16x16x32_f16 v[190:193], v[242:245], v[218:221], v[190:193]
	v_mfma_f32_16x16x32_f16 v[202:205], v[242:245], v[222:225], v[202:205]
	v_mfma_f32_16x16x32_f16 v[206:209], v[242:245], v[226:229], v[206:209]
	v_mfma_f32_16x16x32_f16 v[214:217], v[242:245], v[230:233], v[214:217]
	s_setprio 0
	s_waitcnt vmcnt(6)
	s_waitcnt lgkmcnt(0)
	s_barrier
	ds_read_b128 v[218:221], v131 offset:32768
	ds_read_b128 v[222:225], v131 offset:34816
	ds_read_b128 v[226:229], v131 offset:36864
	ds_read_b128 v[230:233], v131 offset:38912
	ds_read_b128 v[8:11], v129 offset:32768
	ds_read_b128 v[18:21], v129 offset:34816
	s_add_u32 s0, s22, 0x600
	s_addc_u32 s1, s90, 0
	v_lshl_add_u64 v[34:35], s[34:35], 0, v[196:197]
	s_mov_b32 m0, s70
	v_cvt_pk_f16_f32 v3, v2, v3
	global_load_lds_dwordx4 v[34:35], off
	v_cvt_pk_f16_f32 v2, v0, v1
	ds_write_b64 v100, v[2:3]
	s_setprio 1
	s_waitcnt lgkmcnt(1)
	v_mfma_f32_16x16x32_f16 v[30:33], v[8:11], v[222:225], v[30:33]
	v_mfma_f32_16x16x32_f16 v[104:107], v[8:11], v[226:229], v[104:107]
	v_mfma_f32_16x16x32_f16 v[108:111], v[18:21], v[218:221], v[108:111]
	v_mfma_f32_16x16x32_f16 v[112:115], v[18:21], v[222:225], v[112:115]
	v_mfma_f32_16x16x32_f16 v[116:119], v[18:21], v[226:229], v[116:119]
	v_mfma_f32_16x16x32_f16 v[242:245], v[8:11], v[218:221], v[14:17]
	v_mfma_f32_16x16x32_f16 v[234:237], v[8:11], v[230:233], v[234:237]
	v_mfma_f32_16x16x32_f16 v[238:241], v[18:21], v[230:233], v[238:241]
	s_setprio 0
	ds_read_b128 v[12:15], v129 offset:36864
	ds_read_b128 v[16:19], v129 offset:38912
	s_mov_b32 m0, s73
	v_lshl_add_u64 v[8:9], v[34:35], 0, s[58:59]
	global_load_lds_dwordx4 v[8:9], off
	v_cvt_pk_f16_f32 v9, v44, v45
	v_cvt_pk_f16_f32 v8, v42, v43
	ds_write_b64 v100, v[8:9] offset:4096
	s_add_u32 s0, s22, 0x20600
	s_addc_u32 s1, s90, 0
	s_add_u32 s100, s22, 0x600
	s_addc_u32 s101, s90, 0
	global_load_dwordx4 v[0:3], v201, s[100:101] nt
	s_setprio 1
	s_waitcnt lgkmcnt(1)
	v_mfma_f32_16x16x32_f16 v[40:43], v[12:15], v[218:221], v[26:29]
	v_mfma_f32_16x16x32_f16 v[120:123], v[12:15], v[230:233], v[120:123]
	v_mfma_f32_16x16x32_f16 v[124:127], v[16:19], v[218:221], v[124:127]
	v_mfma_f32_16x16x32_f16 v[146:149], v[16:19], v[222:225], v[146:149]
	v_mfma_f32_16x16x32_f16 v[134:137], v[16:19], v[230:233], v[134:137]
	v_mfma_f32_16x16x32_f16 v[138:141], v[12:15], v[222:225], v[138:141]
	v_mfma_f32_16x16x32_f16 v[142:145], v[12:15], v[226:229], v[142:145]
	v_mfma_f32_16x16x32_f16 v[150:153], v[16:19], v[226:229], v[150:153]
	s_setprio 0
	ds_read_b128 v[16:19], v129 offset:40960
	ds_read_b128 v[26:29], v129 offset:43008
	s_mov_b32 m0, s91
	v_lshl_add_u64 v[12:13], v[34:35], 0, s[60:61]
	global_load_lds_dwordx4 v[12:13], off
	v_cvt_pk_f16_f32 v13, v48, v49
	v_cvt_pk_f16_f32 v12, v46, v47
	ds_write_b64 v100, v[12:13] offset:8192
	s_add_u32 s0, s22, 0x40600
	s_addc_u32 s1, s90, 0
	s_add_u32 s100, s22, 0x20600
	s_addc_u32 s101, s90, 0
	global_load_dwordx4 v[8:11], v201, s[100:101] nt
	s_setprio 1
	s_waitcnt lgkmcnt(1)
	v_mfma_f32_16x16x32_f16 v[44:47], v[16:19], v[218:221], v[22:25]
	v_mfma_f32_16x16x32_f16 v[170:173], v[16:19], v[222:225], v[170:173]
	v_mfma_f32_16x16x32_f16 v[174:177], v[16:19], v[226:229], v[174:177]
	v_mfma_f32_16x16x32_f16 v[162:165], v[16:19], v[230:233], v[162:165]
	v_mfma_f32_16x16x32_f16 v[178:181], v[26:29], v[218:221], v[178:181]
	v_mfma_f32_16x16x32_f16 v[182:185], v[26:29], v[222:225], v[182:185]
	v_mfma_f32_16x16x32_f16 v[186:189], v[26:29], v[226:229], v[186:189]
	v_mfma_f32_16x16x32_f16 v[154:157], v[26:29], v[230:233], v[154:157]
	s_setprio 0
	ds_read_b128 v[20:23], v129 offset:45056
	ds_read_b128 v[24:27], v129 offset:47104
	s_mov_b32 m0, s92
	v_lshl_add_u64 v[16:17], v[34:35], 0, s[62:63]
	global_load_lds_dwordx4 v[16:17], off
	v_cvt_pk_f16_f32 v17, v76, v77
	v_cvt_pk_f16_f32 v16, v74, v75
	ds_write_b64 v100, v[16:17] offset:12288
	s_add_u32 s0, s22, 0x60600
	s_addc_u32 s1, s90, 0
	s_add_u32 s100, s22, 0x40600
	s_addc_u32 s101, s90, 0
	global_load_dwordx4 v[12:15], v201, s[100:101] nt
	s_setprio 1
	s_waitcnt lgkmcnt(1)
	v_mfma_f32_16x16x32_f16 v[74:77], v[20:23], v[218:221], v[246:249]
	v_mfma_f32_16x16x32_f16 v[158:161], v[20:23], v[222:225], v[158:161]
	v_mfma_f32_16x16x32_f16 v[210:213], v[20:23], v[226:229], v[210:213]
	v_mfma_f32_16x16x32_f16 v[166:169], v[20:23], v[230:233], v[166:169]
	v_mfma_f32_16x16x32_f16 v[190:193], v[24:27], v[218:221], v[190:193]
	v_mfma_f32_16x16x32_f16 v[202:205], v[24:27], v[222:225], v[202:205]
	v_mfma_f32_16x16x32_f16 v[206:209], v[24:27], v[226:229], v[206:209]
	v_mfma_f32_16x16x32_f16 v[214:217], v[24:27], v[230:233], v[214:217]
	s_setprio 0
	ds_read_b128 v[218:221], v128 offset:32768
	ds_read_b128 v[222:225], v128 offset:34816
	ds_read_b128 v[226:229], v128 offset:36864
	ds_read_b128 v[230:233], v128 offset:38912
	ds_read_b128 v[24:27], v130 offset:32768
	ds_read_b128 v[246:249], v130 offset:34816
	v_cvt_pk_f16_f32 v21, v80, v81
	v_cvt_pk_f16_f32 v20, v78, v79
	ds_write_b64 v100, v[20:21] offset:16384
	s_add_u32 s0, s22, 0x80600
	s_addc_u32 s1, s90, 0
	s_add_u32 s100, s22, 0x60600
	s_addc_u32 s101, s90, 0
	global_load_dwordx4 v[16:19], v201, s[100:101] nt
	s_setprio 1
	s_waitcnt lgkmcnt(1)
	v_mfma_f32_16x16x32_f16 v[78:81], v[24:27], v[218:221], v[242:245]
	v_mfma_f32_16x16x32_f16 v[104:107], v[24:27], v[226:229], v[104:107]
	v_mfma_f32_16x16x32_f16 v[108:111], v[246:249], v[218:221], v[108:111]
	v_mfma_f32_16x16x32_f16 v[112:115], v[246:249], v[222:225], v[112:115]
	v_mfma_f32_16x16x32_f16 v[116:119], v[246:249], v[226:229], v[116:119]
	v_mfma_f32_16x16x32_f16 v[242:245], v[24:27], v[222:225], v[30:33]
	v_mfma_f32_16x16x32_f16 v[234:237], v[24:27], v[230:233], v[234:237]
	v_mfma_f32_16x16x32_f16 v[238:241], v[246:249], v[230:233], v[238:241]
	s_setprio 0
	ds_read_b128 v[28:31], v130 offset:36864
	ds_read_b128 v[32:35], v130 offset:38912
	v_cvt_pk_f16_f32 v25, v84, v85
	v_cvt_pk_f16_f32 v24, v82, v83
	ds_write_b64 v100, v[24:25] offset:20480
	s_add_u32 s0, s22, 0xa0600
	s_addc_u32 s1, s90, 0
	s_add_u32 s100, s22, 0x80600
	s_addc_u32 s101, s90, 0
	global_load_dwordx4 v[20:23], v201, s[100:101] nt
	s_setprio 1
	s_waitcnt lgkmcnt(1)
	v_mfma_f32_16x16x32_f16 v[82:85], v[28:31], v[218:221], v[40:43]
	v_mfma_f32_16x16x32_f16 v[120:123], v[28:31], v[230:233], v[120:123]
	v_mfma_f32_16x16x32_f16 v[124:127], v[32:35], v[218:221], v[124:127]
	v_mfma_f32_16x16x32_f16 v[146:149], v[32:35], v[222:225], v[146:149]
	v_mfma_f32_16x16x32_f16 v[134:137], v[32:35], v[230:233], v[134:137]
	v_mfma_f32_16x16x32_f16 v[138:141], v[28:31], v[222:225], v[138:141]
	v_mfma_f32_16x16x32_f16 v[142:145], v[28:31], v[226:229], v[142:145]
	v_mfma_f32_16x16x32_f16 v[150:153], v[32:35], v[226:229], v[150:153]
	s_setprio 0
	ds_read_b128 v[32:35], v130 offset:40960
	ds_read_b128 v[40:43], v130 offset:43008
	v_cvt_pk_f16_f32 v29, v88, v89
	v_cvt_pk_f16_f32 v28, v86, v87
	ds_write_b64 v100, v[28:29] offset:24576
	s_add_u32 s0, s22, 0xc0600
	s_addc_u32 s1, s90, 0
	s_add_u32 s100, s22, 0xa0600
	s_addc_u32 s101, s90, 0
	global_load_dwordx4 v[24:27], v201, s[100:101] nt
	s_add_u32 s100, s22, 0xc0600
	s_addc_u32 s101, s90, 0
	global_load_dwordx4 v[28:31], v201, s[100:101] nt
	s_setprio 1
	s_waitcnt lgkmcnt(1)
	v_mfma_f32_16x16x32_f16 v[86:89], v[32:35], v[218:221], v[44:47]
	v_mfma_f32_16x16x32_f16 v[170:173], v[32:35], v[222:225], v[170:173]
	v_mfma_f32_16x16x32_f16 v[174:177], v[32:35], v[226:229], v[174:177]
	v_mfma_f32_16x16x32_f16 v[162:165], v[32:35], v[230:233], v[162:165]
	v_mfma_f32_16x16x32_f16 v[178:181], v[40:43], v[218:221], v[178:181]
	v_mfma_f32_16x16x32_f16 v[182:185], v[40:43], v[222:225], v[182:185]
	v_mfma_f32_16x16x32_f16 v[186:189], v[40:43], v[226:229], v[186:189]
	v_mfma_f32_16x16x32_f16 v[154:157], v[40:43], v[230:233], v[154:157]
	s_setprio 0
	ds_read_b128 v[40:43], v130 offset:45056
	ds_read_b128 v[44:47], v130 offset:47104
	v_cvt_pk_f16_f32 v33, v92, v93
	v_cvt_pk_f16_f32 v32, v90, v91
	ds_write_b64 v100, v[32:33] offset:28672
	s_add_u32 s0, s22, 0xe0600
	s_addc_u32 s1, s90, 0
	s_add_u32 s100, s22, 0xe0600
	s_addc_u32 s101, s90, 0
	global_load_dwordx4 v[32:35], v201, s[100:101] nt
	s_setprio 1
	s_waitcnt lgkmcnt(1)
	v_mfma_f32_16x16x32_f16 v[74:77], v[40:43], v[218:221], v[74:77]
	v_mfma_f32_16x16x32_f16 v[90:93], v[40:43], v[222:225], v[158:161]
	v_mfma_f32_16x16x32_f16 v[158:161], v[40:43], v[226:229], v[210:213]
	v_mfma_f32_16x16x32_f16 v[166:169], v[40:43], v[230:233], v[166:169]
	v_mfma_f32_16x16x32_f16 v[190:193], v[44:47], v[218:221], v[190:193]
	v_mfma_f32_16x16x32_f16 v[202:205], v[44:47], v[222:225], v[202:205]
	v_mfma_f32_16x16x32_f16 v[206:209], v[44:47], v[226:229], v[206:209]
	v_mfma_f32_16x16x32_f16 v[210:213], v[44:47], v[230:233], v[214:217]
	s_setprio 0
	s_waitcnt vmcnt(6)
	s_waitcnt lgkmcnt(0)
	s_barrier
	s_nop 0
	ds_read_b128 v[214:217], v131
	ds_read_b128 v[218:221], v131 offset:2048
	ds_read_b128 v[222:225], v131 offset:4096
	ds_read_b128 v[226:229], v131 offset:6144
	ds_read_b128 v[40:43], v129
	ds_read_b128 v[44:47], v129 offset:2048
	s_add_u32 s70, s22, 0x700
	s_addc_u32 s71, s90, 0
	v_lshl_add_u64 v[198:199], s[36:37], 0, v[196:197]
	v_readfirstlane_b32 s0, v95
	s_mov_b32 m0, s0
	v_cvt_pk_f16_f32 v7, v6, v7
	global_load_lds_dwordx4 v[198:199], off
	v_cvt_pk_f16_f32 v6, v4, v5
	ds_write_b64 v100, v[6:7] offset:32768
	s_setprio 1
	s_waitcnt lgkmcnt(1)
	v_mfma_f32_16x16x32_f16 v[78:81], v[40:43], v[214:217], v[78:81]
	v_mfma_f32_16x16x32_f16 v[104:107], v[40:43], v[222:225], v[104:107]
	v_mfma_f32_16x16x32_f16 v[108:111], v[44:47], v[214:217], v[108:111]
	v_mfma_f32_16x16x32_f16 v[112:115], v[44:47], v[218:221], v[112:115]
	v_mfma_f32_16x16x32_f16 v[116:119], v[44:47], v[222:225], v[116:119]
	v_mfma_f32_16x16x32_f16 v[230:233], v[40:43], v[218:221], v[242:245]
	v_mfma_f32_16x16x32_f16 v[234:237], v[40:43], v[226:229], v[234:237]
	v_mfma_f32_16x16x32_f16 v[238:241], v[44:47], v[226:229], v[238:241]
	s_setprio 0
	ds_read_b128 v[44:47], v129 offset:4096
	ds_read_b128 v[242:245], v129 offset:6144
	v_readfirstlane_b32 s72, v96
	v_lshl_add_u64 v[40:41], v[198:199], 0, s[58:59]
	s_mov_b32 m0, s72
	s_nop 0
	global_load_lds_dwordx4 v[40:41], off
	v_cvt_pk_f16_f32 v41, v52, v53
	v_cvt_pk_f16_f32 v40, v50, v51
	ds_write_b64 v100, v[40:41] offset:36864
	s_add_u32 s70, s22, 0x20700
	s_addc_u32 s71, s90, 0
	s_add_u32 s100, s22, 0x700
	s_addc_u32 s101, s90, 0
	global_load_dwordx4 v[4:7], v201, s[100:101] nt
	s_setprio 1
	s_waitcnt lgkmcnt(1)
	v_mfma_f32_16x16x32_f16 v[82:85], v[44:47], v[214:217], v[82:85]
	v_mfma_f32_16x16x32_f16 v[120:123], v[44:47], v[226:229], v[120:123]
	v_mfma_f32_16x16x32_f16 v[124:127], v[242:245], v[214:217], v[124:127]
	v_mfma_f32_16x16x32_f16 v[146:149], v[242:245], v[218:221], v[146:149]
	v_mfma_f32_16x16x32_f16 v[134:137], v[242:245], v[226:229], v[134:137]
	v_mfma_f32_16x16x32_f16 v[138:141], v[44:47], v[218:221], v[138:141]
	v_mfma_f32_16x16x32_f16 v[142:145], v[44:47], v[222:225], v[142:145]
	v_mfma_f32_16x16x32_f16 v[150:153], v[242:245], v[222:225], v[150:153]
	s_setprio 0
	ds_read_b128 v[48:51], v129 offset:8192
	ds_read_b128 v[242:245], v129 offset:10240
	v_readfirstlane_b32 s71, v97
	v_lshl_add_u64 v[44:45], v[198:199], 0, s[60:61]
	s_mov_b32 m0, s71
	s_nop 0
	global_load_lds_dwordx4 v[44:45], off
	v_cvt_pk_f16_f32 v45, v56, v57
	v_cvt_pk_f16_f32 v44, v54, v55
	ds_write_b64 v100, v[44:45] offset:40960
	s_add_u32 s80, s22, 0x40700
	s_addc_u32 s81, s90, 0
	s_add_u32 s100, s22, 0x20700
	s_addc_u32 s101, s90, 0
	global_load_dwordx4 v[40:43], v201, s[100:101] nt
	s_setprio 1
	s_waitcnt lgkmcnt(1)
	v_mfma_f32_16x16x32_f16 v[86:89], v[48:51], v[214:217], v[86:89]
	v_mfma_f32_16x16x32_f16 v[170:173], v[48:51], v[218:221], v[170:173]
	v_mfma_f32_16x16x32_f16 v[174:177], v[48:51], v[222:225], v[174:177]
	v_mfma_f32_16x16x32_f16 v[162:165], v[48:51], v[226:229], v[162:165]
	v_mfma_f32_16x16x32_f16 v[178:181], v[242:245], v[214:217], v[178:181]
	v_mfma_f32_16x16x32_f16 v[182:185], v[242:245], v[218:221], v[182:185]
	v_mfma_f32_16x16x32_f16 v[186:189], v[242:245], v[222:225], v[186:189]
	v_mfma_f32_16x16x32_f16 v[154:157], v[242:245], v[226:229], v[154:157]
	s_setprio 0
	ds_read_b128 v[52:55], v129 offset:12288
	ds_read_b128 v[242:245], v129 offset:14336
	v_readfirstlane_b32 s70, v98
	v_lshl_add_u64 v[48:49], v[198:199], 0, s[62:63]
	s_mov_b32 m0, s70
	s_nop 0
	global_load_lds_dwordx4 v[48:49], off
	v_cvt_pk_f16_f32 v49, v60, v61
	v_cvt_pk_f16_f32 v48, v58, v59
	ds_write_b64 v100, v[48:49] offset:45056
	s_add_u32 s80, s22, 0x60700
	s_addc_u32 s81, s90, 0
	s_add_u32 s100, s22, 0x40700
	s_addc_u32 s101, s90, 0
	global_load_dwordx4 v[44:47], v201, s[100:101] nt
	s_setprio 1
	s_waitcnt lgkmcnt(1)
	v_mfma_f32_16x16x32_f16 v[74:77], v[52:55], v[214:217], v[74:77]
	v_mfma_f32_16x16x32_f16 v[90:93], v[52:55], v[218:221], v[90:93]
	v_mfma_f32_16x16x32_f16 v[158:161], v[52:55], v[222:225], v[158:161]
	v_mfma_f32_16x16x32_f16 v[166:169], v[52:55], v[226:229], v[166:169]
	v_mfma_f32_16x16x32_f16 v[190:193], v[242:245], v[214:217], v[190:193]
	v_mfma_f32_16x16x32_f16 v[202:205], v[242:245], v[218:221], v[202:205]
	v_mfma_f32_16x16x32_f16 v[206:209], v[242:245], v[222:225], v[206:209]
	v_mfma_f32_16x16x32_f16 v[210:213], v[242:245], v[226:229], v[210:213]
	s_setprio 0
	ds_read_b128 v[214:217], v128
	ds_read_b128 v[218:221], v128 offset:2048
	ds_read_b128 v[222:225], v128 offset:4096
	ds_read_b128 v[226:229], v128 offset:6144
	ds_read_b128 v[56:59], v130
	ds_read_b128 v[242:245], v130 offset:2048
	v_cvt_pk_f16_f32 v53, v64, v65
	v_cvt_pk_f16_f32 v52, v62, v63
	ds_write_b64 v100, v[52:53] offset:49152
	s_add_u32 s80, s22, 0x80700
	s_addc_u32 s81, s90, 0
	s_add_u32 s100, s22, 0x60700
	s_addc_u32 s101, s90, 0
	global_load_dwordx4 v[48:51], v201, s[100:101] nt
	s_setprio 1
	s_waitcnt lgkmcnt(1)
	v_mfma_f32_16x16x32_f16 v[78:81], v[56:59], v[214:217], v[78:81]
	v_mfma_f32_16x16x32_f16 v[104:107], v[56:59], v[222:225], v[104:107]
	v_mfma_f32_16x16x32_f16 v[108:111], v[242:245], v[214:217], v[108:111]
	v_mfma_f32_16x16x32_f16 v[112:115], v[242:245], v[218:221], v[112:115]
	v_mfma_f32_16x16x32_f16 v[116:119], v[242:245], v[222:225], v[116:119]
	v_mfma_f32_16x16x32_f16 v[230:233], v[56:59], v[218:221], v[230:233]
	v_mfma_f32_16x16x32_f16 v[234:237], v[56:59], v[226:229], v[234:237]
	v_mfma_f32_16x16x32_f16 v[238:241], v[242:245], v[226:229], v[238:241]
	s_setprio 0
	ds_read_b128 v[60:63], v130 offset:4096
	ds_read_b128 v[242:245], v130 offset:6144
	v_cvt_pk_f16_f32 v57, v68, v69
	v_cvt_pk_f16_f32 v56, v66, v67
	ds_write_b64 v100, v[56:57] offset:53248
	s_add_u32 s80, s22, 0xa0700
	s_addc_u32 s81, s90, 0
	s_add_u32 s100, s22, 0x80700
	s_addc_u32 s101, s90, 0
	global_load_dwordx4 v[52:55], v201, s[100:101] nt
	s_setprio 1
	s_waitcnt lgkmcnt(1)
	v_mfma_f32_16x16x32_f16 v[82:85], v[60:63], v[214:217], v[82:85]
	v_mfma_f32_16x16x32_f16 v[120:123], v[60:63], v[226:229], v[120:123]
	v_mfma_f32_16x16x32_f16 v[124:127], v[242:245], v[214:217], v[124:127]
	v_mfma_f32_16x16x32_f16 v[146:149], v[242:245], v[218:221], v[146:149]
	v_mfma_f32_16x16x32_f16 v[134:137], v[242:245], v[226:229], v[134:137]
	v_mfma_f32_16x16x32_f16 v[138:141], v[60:63], v[218:221], v[138:141]
	v_mfma_f32_16x16x32_f16 v[142:145], v[60:63], v[222:225], v[142:145]
	v_mfma_f32_16x16x32_f16 v[150:153], v[242:245], v[222:225], v[150:153]
	s_setprio 0
	ds_read_b128 v[64:67], v130 offset:8192
	ds_read_b128 v[242:245], v130 offset:10240
	v_cvt_pk_f16_f32 v61, v72, v73
	v_cvt_pk_f16_f32 v60, v70, v71
	ds_write_b64 v100, v[60:61] offset:57344
	s_add_u32 s80, s22, 0xc0700
	s_addc_u32 s81, s90, 0
	s_add_u32 s100, s22, 0xa0700
	s_addc_u32 s101, s90, 0
	global_load_dwordx4 v[56:59], v201, s[100:101] nt
	s_add_u32 s100, s22, 0xc0700
	s_addc_u32 s101, s90, 0
	global_load_dwordx4 v[60:63], v201, s[100:101] nt
	s_setprio 1
	s_waitcnt lgkmcnt(1)
	v_mfma_f32_16x16x32_f16 v[86:89], v[64:67], v[214:217], v[86:89]
	v_mfma_f32_16x16x32_f16 v[170:173], v[64:67], v[218:221], v[170:173]
	v_mfma_f32_16x16x32_f16 v[174:177], v[64:67], v[222:225], v[174:177]
	v_mfma_f32_16x16x32_f16 v[162:165], v[64:67], v[226:229], v[162:165]
	v_mfma_f32_16x16x32_f16 v[178:181], v[242:245], v[214:217], v[178:181]
	v_mfma_f32_16x16x32_f16 v[182:185], v[242:245], v[218:221], v[182:185]
	v_mfma_f32_16x16x32_f16 v[186:189], v[242:245], v[222:225], v[186:189]
	v_mfma_f32_16x16x32_f16 v[154:157], v[242:245], v[226:229], v[154:157]
	s_setprio 0
	ds_read_b128 v[64:67], v130 offset:12288
	ds_read_b128 v[68:71], v130 offset:14336
	v_cvt_pk_f16_f32 v39, v38, v39
	v_cvt_pk_f16_f32 v38, v36, v37
	ds_write_b64 v100, v[38:39] offset:61440
	s_add_u32 s80, s22, 0xe0700
	s_addc_u32 s81, s90, 0
	s_add_u32 s100, s22, 0xe0700
	s_addc_u32 s101, s90, 0
	global_load_dwordx4 v[36:39], v201, s[100:101] nt
	s_setprio 1
	s_waitcnt lgkmcnt(1)
	v_mfma_f32_16x16x32_f16 v[90:93], v[64:67], v[218:221], v[90:93]
	v_mfma_f32_16x16x32_f16 v[242:245], v[64:67], v[214:217], v[74:77]
	v_mfma_f32_16x16x32_f16 v[158:161], v[64:67], v[222:225], v[158:161]
	v_mfma_f32_16x16x32_f16 v[166:169], v[64:67], v[226:229], v[166:169]
	v_mfma_f32_16x16x32_f16 v[190:193], v[68:71], v[214:217], v[190:193]
	v_mfma_f32_16x16x32_f16 v[202:205], v[68:71], v[218:221], v[202:205]
	v_mfma_f32_16x16x32_f16 v[206:209], v[68:71], v[222:225], v[206:209]
	v_mfma_f32_16x16x32_f16 v[210:213], v[68:71], v[226:229], v[210:213]
	s_setprio 0
	s_waitcnt vmcnt(6)
	s_waitcnt lgkmcnt(0)
	s_barrier
	ds_read_b128 v[214:217], v131 offset:32768
	ds_read_b128 v[218:221], v131 offset:34816
	ds_read_b128 v[222:225], v131 offset:36864
	ds_read_b128 v[226:229], v131 offset:38912
	ds_read_b128 v[64:67], v129 offset:32768
	ds_read_b128 v[68:71], v129 offset:34816
	s_add_u32 s80, s22, 0x800
	s_addc_u32 s81, s90, 0
	v_lshl_add_u64 v[198:199], s[38:39], 0, v[196:197]
	v_readfirstlane_b32 s1, v94
	s_mov_b32 m0, s1
	v_cvt_pk_f16_f32 v3, v2, v3
	global_load_lds_dwordx4 v[198:199], off
	v_cvt_pk_f16_f32 v2, v0, v1
	ds_write_b64 v100, v[2:3]
	s_setprio 1
	s_waitcnt lgkmcnt(1)
	v_mfma_f32_16x16x32_f16 v[104:107], v[64:67], v[222:225], v[104:107]
	v_mfma_f32_16x16x32_f16 v[108:111], v[68:71], v[214:217], v[108:111]
	v_mfma_f32_16x16x32_f16 v[112:115], v[68:71], v[218:221], v[112:115]
	v_mfma_f32_16x16x32_f16 v[116:119], v[68:71], v[222:225], v[116:119]
	v_mfma_f32_16x16x32_f16 v[246:249], v[64:67], v[214:217], v[78:81]
	v_mfma_f32_16x16x32_f16 v[230:233], v[64:67], v[218:221], v[230:233]
	v_mfma_f32_16x16x32_f16 v[234:237], v[64:67], v[226:229], v[234:237]
	v_mfma_f32_16x16x32_f16 v[238:241], v[68:71], v[226:229], v[238:241]
	s_setprio 0
	ds_read_b128 v[68:71], v129 offset:36864
	ds_read_b128 v[72:75], v129 offset:38912
	v_readfirstlane_b32 s92, v99
	v_lshl_add_u64 v[64:65], v[198:199], 0, s[58:59]
	s_mov_b32 m0, s92
	v_cvt_pk_f16_f32 v11, v10, v11
	global_load_lds_dwordx4 v[64:65], off
	v_cvt_pk_f16_f32 v10, v8, v9
	ds_write_b64 v100, v[10:11] offset:4096
	s_add_u32 s80, s22, 0x20800
	s_addc_u32 s81, s90, 0
	s_add_u32 s100, s22, 0x800
	s_addc_u32 s101, s90, 0
	global_load_dwordx4 v[0:3], v201, s[100:101] nt
	s_setprio 1
	s_waitcnt lgkmcnt(1)
	v_mfma_f32_16x16x32_f16 v[8:11], v[68:71], v[214:217], v[82:85]
	v_mfma_f32_16x16x32_f16 v[120:123], v[68:71], v[226:229], v[120:123]
	v_mfma_f32_16x16x32_f16 v[124:127], v[72:75], v[214:217], v[124:127]
	v_mfma_f32_16x16x32_f16 v[146:149], v[72:75], v[218:221], v[146:149]
	v_mfma_f32_16x16x32_f16 v[134:137], v[72:75], v[226:229], v[134:137]
	v_mfma_f32_16x16x32_f16 v[138:141], v[68:71], v[218:221], v[138:141]
	v_mfma_f32_16x16x32_f16 v[142:145], v[68:71], v[222:225], v[142:145]
	v_mfma_f32_16x16x32_f16 v[150:153], v[72:75], v[222:225], v[150:153]
	s_setprio 0
	ds_read_b128 v[72:75], v129 offset:40960
	ds_read_b128 v[76:79], v129 offset:43008
	v_readfirstlane_b32 s91, v101
	v_lshl_add_u64 v[68:69], v[198:199], 0, s[60:61]
	s_mov_b32 m0, s91
	v_cvt_pk_f16_f32 v15, v14, v15
	global_load_lds_dwordx4 v[68:69], off
	v_cvt_pk_f16_f32 v14, v12, v13
	ds_write_b64 v100, v[14:15] offset:8192
	s_add_u32 s80, s22, 0x40800
	s_addc_u32 s81, s90, 0
	s_add_u32 s100, s22, 0x20800
	s_addc_u32 s101, s90, 0
	global_load_dwordx4 v[64:67], v201, s[100:101] nt
	s_setprio 1
	s_waitcnt lgkmcnt(1)
	v_mfma_f32_16x16x32_f16 v[12:15], v[72:75], v[214:217], v[86:89]
	v_mfma_f32_16x16x32_f16 v[170:173], v[72:75], v[218:221], v[170:173]
	v_mfma_f32_16x16x32_f16 v[174:177], v[72:75], v[222:225], v[174:177]
	v_mfma_f32_16x16x32_f16 v[162:165], v[72:75], v[226:229], v[162:165]
	v_mfma_f32_16x16x32_f16 v[178:181], v[76:79], v[214:217], v[178:181]
	v_mfma_f32_16x16x32_f16 v[182:185], v[76:79], v[218:221], v[182:185]
	v_mfma_f32_16x16x32_f16 v[186:189], v[76:79], v[222:225], v[186:189]
	v_mfma_f32_16x16x32_f16 v[154:157], v[76:79], v[226:229], v[154:157]
	s_setprio 0
	ds_read_b128 v[76:79], v129 offset:45056
	ds_read_b128 v[80:83], v129 offset:47104
	v_readfirstlane_b32 s73, v102
	v_lshl_add_u64 v[72:73], v[198:199], 0, s[62:63]
	s_mov_b32 m0, s73
	v_cvt_pk_f16_f32 v19, v18, v19
	global_load_lds_dwordx4 v[72:73], off
	v_cvt_pk_f16_f32 v18, v16, v17
	ds_write_b64 v100, v[18:19] offset:12288
	s_add_u32 s80, s22, 0x60800
	s_addc_u32 s81, s90, 0
	s_add_u32 s100, s22, 0x40800
	s_addc_u32 s101, s90, 0
	global_load_dwordx4 v[68:71], v201, s[100:101] nt
	s_setprio 1
	s_waitcnt lgkmcnt(1)
	v_mfma_f32_16x16x32_f16 v[16:19], v[76:79], v[214:217], v[242:245]
	v_mfma_f32_16x16x32_f16 v[242:245], v[76:79], v[218:221], v[90:93]
	v_mfma_f32_16x16x32_f16 v[158:161], v[76:79], v[222:225], v[158:161]
	v_mfma_f32_16x16x32_f16 v[166:169], v[76:79], v[226:229], v[166:169]
	v_mfma_f32_16x16x32_f16 v[190:193], v[80:83], v[214:217], v[190:193]
	v_mfma_f32_16x16x32_f16 v[202:205], v[80:83], v[218:221], v[202:205]
	v_mfma_f32_16x16x32_f16 v[206:209], v[80:83], v[222:225], v[206:209]
	v_mfma_f32_16x16x32_f16 v[210:213], v[80:83], v[226:229], v[210:213]
	s_setprio 0
	ds_read_b128 v[214:217], v128 offset:32768
	ds_read_b128 v[218:221], v128 offset:34816
	ds_read_b128 v[222:225], v128 offset:36864
	ds_read_b128 v[226:229], v128 offset:38912
	ds_read_b128 v[80:83], v130 offset:32768
	ds_read_b128 v[84:87], v130 offset:34816
	v_cvt_pk_f16_f32 v23, v22, v23
	v_cvt_pk_f16_f32 v22, v20, v21
	ds_write_b64 v100, v[22:23] offset:16384
	s_add_u32 s80, s22, 0x80800
	s_addc_u32 s81, s90, 0
	s_add_u32 s100, s22, 0x60800
	s_addc_u32 s101, s90, 0
	global_load_dwordx4 v[72:75], v201, s[100:101] nt
	s_setprio 1
	s_waitcnt lgkmcnt(1)
	v_mfma_f32_16x16x32_f16 v[20:23], v[80:83], v[214:217], v[246:249]
	v_mfma_f32_16x16x32_f16 v[104:107], v[80:83], v[222:225], v[104:107]
	v_mfma_f32_16x16x32_f16 v[108:111], v[84:87], v[214:217], v[108:111]
	v_mfma_f32_16x16x32_f16 v[112:115], v[84:87], v[218:221], v[112:115]
	v_mfma_f32_16x16x32_f16 v[116:119], v[84:87], v[222:225], v[116:119]
	v_mfma_f32_16x16x32_f16 v[230:233], v[80:83], v[218:221], v[230:233]
	v_mfma_f32_16x16x32_f16 v[234:237], v[80:83], v[226:229], v[234:237]
	v_mfma_f32_16x16x32_f16 v[238:241], v[84:87], v[226:229], v[238:241]
	s_setprio 0
	ds_read_b128 v[84:87], v130 offset:36864
	ds_read_b128 v[88:91], v130 offset:38912
	v_cvt_pk_f16_f32 v27, v26, v27
	v_cvt_pk_f16_f32 v26, v24, v25
	ds_write_b64 v100, v[26:27] offset:20480
	s_add_u32 s80, s22, 0xa0800
	s_addc_u32 s81, s90, 0
	s_add_u32 s100, s22, 0x80800
	s_addc_u32 s101, s90, 0
	global_load_dwordx4 v[76:79], v201, s[100:101] nt
	s_setprio 1
	s_waitcnt lgkmcnt(1)
	v_mfma_f32_16x16x32_f16 v[24:27], v[84:87], v[214:217], v[8:11]
	v_mfma_f32_16x16x32_f16 v[120:123], v[84:87], v[226:229], v[120:123]
	v_mfma_f32_16x16x32_f16 v[124:127], v[88:91], v[214:217], v[124:127]
	v_mfma_f32_16x16x32_f16 v[146:149], v[88:91], v[218:221], v[146:149]
	v_mfma_f32_16x16x32_f16 v[134:137], v[88:91], v[226:229], v[134:137]
	v_mfma_f32_16x16x32_f16 v[138:141], v[84:87], v[218:221], v[138:141]
	v_mfma_f32_16x16x32_f16 v[142:145], v[84:87], v[222:225], v[142:145]
	v_mfma_f32_16x16x32_f16 v[150:153], v[88:91], v[222:225], v[150:153]
	s_setprio 0
	ds_read_b128 v[8:11], v130 offset:40960
	ds_read_b128 v[88:91], v130 offset:43008
	v_cvt_pk_f16_f32 v31, v30, v31
	v_cvt_pk_f16_f32 v30, v28, v29
	ds_write_b64 v100, v[30:31] offset:24576
	s_add_u32 s80, s22, 0xc0800
	s_addc_u32 s81, s90, 0
	s_add_u32 s100, s22, 0xa0800
	s_addc_u32 s101, s90, 0
	global_load_dwordx4 v[80:83], v201, s[100:101] nt
	s_add_u32 s100, s22, 0xc0800
	s_addc_u32 s101, s90, 0
	global_load_dwordx4 v[84:87], v201, s[100:101] nt
	s_setprio 1
	s_waitcnt lgkmcnt(1)
	v_mfma_f32_16x16x32_f16 v[12:15], v[8:11], v[214:217], v[12:15]
	v_mfma_f32_16x16x32_f16 v[28:31], v[8:11], v[218:221], v[170:173]
	v_mfma_f32_16x16x32_f16 v[170:173], v[8:11], v[222:225], v[174:177]
	v_mfma_f32_16x16x32_f16 v[162:165], v[8:11], v[226:229], v[162:165]
	v_mfma_f32_16x16x32_f16 v[174:177], v[88:91], v[214:217], v[178:181]
	v_mfma_f32_16x16x32_f16 v[178:181], v[88:91], v[218:221], v[182:185]
	v_mfma_f32_16x16x32_f16 v[182:185], v[88:91], v[222:225], v[186:189]
	v_mfma_f32_16x16x32_f16 v[154:157], v[88:91], v[226:229], v[154:157]
	s_setprio 0
	ds_read_b128 v[8:11], v130 offset:45056
	ds_read_b128 v[186:189], v130 offset:47104
	v_cvt_pk_f16_f32 v35, v34, v35
	v_cvt_pk_f16_f32 v34, v32, v33
	ds_write_b64 v100, v[34:35] offset:28672
	s_add_u32 s80, s22, 0xe0800
	s_addc_u32 s81, s90, 0
	s_add_u32 s100, s22, 0xe0800
	s_addc_u32 s101, s90, 0
	global_load_dwordx4 v[88:91], v201, s[100:101] nt
	s_setprio 1
	s_waitcnt lgkmcnt(1)
	v_mfma_f32_16x16x32_f16 v[16:19], v[8:11], v[214:217], v[16:19]
	v_mfma_f32_16x16x32_f16 v[32:35], v[8:11], v[218:221], v[242:245]
	v_mfma_f32_16x16x32_f16 v[158:161], v[8:11], v[222:225], v[158:161]
	v_mfma_f32_16x16x32_f16 v[166:169], v[8:11], v[226:229], v[166:169]
	v_mfma_f32_16x16x32_f16 v[190:193], v[186:189], v[214:217], v[190:193]
	v_mfma_f32_16x16x32_f16 v[202:205], v[186:189], v[218:221], v[202:205]
	v_mfma_f32_16x16x32_f16 v[206:209], v[186:189], v[222:225], v[206:209]
	v_mfma_f32_16x16x32_f16 v[186:189], v[186:189], v[226:229], v[210:213]
	s_setprio 0
	s_waitcnt vmcnt(6)
	s_waitcnt lgkmcnt(0)
	s_barrier
	s_nop 0
	ds_read_b128 v[210:213], v131
	ds_read_b128 v[214:217], v131 offset:2048
	ds_read_b128 v[218:221], v131 offset:4096
	ds_read_b128 v[222:225], v131 offset:6144
	ds_read_b128 v[8:11], v129
	ds_read_b128 v[226:229], v129 offset:2048
	s_add_u32 s80, s22, 0x900
	v_lshl_add_u64 v[92:93], s[40:41], 0, v[196:197]
	s_addc_u32 s81, s90, 0
	v_cvt_pk_f16_f32 v7, v6, v7
	s_cmp_lg_u32 s2, 0
	s_cbranch_scc1 .Lres_skip_0
	s_add_u32 m0, s0, 0x18000
	s_nop 0
	global_load_lds_dwordx4 v[92:93], off

.Lres_skip_3:
	v_cvt_pk_f16_f32 v45, v50, v51
	v_cvt_pk_f16_f32 v44, v48, v49
	ds_write_b64 v100, v[44:45] offset:45056
	s_add_u32 s70, s22, 0x60900
	s_addc_u32 s71, s90, 0
	s_add_u32 s100, s22, 0x40900
	s_addc_u32 s101, s90, 0
	global_load_dwordx4 v[40:43], v201, s[100:101] nt
	s_setprio 1
	s_waitcnt lgkmcnt(1)
	v_mfma_f32_16x16x32_f16 v[16:19], v[238:241], v[210:213], v[16:19]
	v_mfma_f32_16x16x32_f16 v[32:35], v[238:241], v[214:217], v[32:35]
	v_mfma_f32_16x16x32_f16 v[158:161], v[238:241], v[218:221], v[158:161]
	v_mfma_f32_16x16x32_f16 v[166:169], v[238:241], v[222:225], v[166:169]
	v_mfma_f32_16x16x32_f16 v[190:193], v[242:245], v[210:213], v[190:193]
	v_mfma_f32_16x16x32_f16 v[202:205], v[242:245], v[214:217], v[202:205]
	v_mfma_f32_16x16x32_f16 v[206:209], v[242:245], v[218:221], v[206:209]
	v_mfma_f32_16x16x32_f16 v[186:189], v[242:245], v[222:225], v[186:189]
	s_setprio 0
	ds_read_b128 v[210:213], v128
	ds_read_b128 v[214:217], v128 offset:2048
	ds_read_b128 v[218:221], v128 offset:4096
	ds_read_b128 v[222:225], v128 offset:6144
	ds_read_b128 v[238:241], v130
	ds_read_b128 v[242:245], v130 offset:2048
	v_cvt_pk_f16_f32 v49, v54, v55
	v_cvt_pk_f16_f32 v48, v52, v53
	ds_write_b64 v100, v[48:49] offset:49152
	s_add_u32 s70, s22, 0x80900
	s_addc_u32 s71, s90, 0
	s_add_u32 s100, s22, 0x60900
	s_addc_u32 s101, s90, 0
	global_load_dwordx4 v[44:47], v201, s[100:101] nt
	s_setprio 1
	s_waitcnt lgkmcnt(1)
	v_mfma_f32_16x16x32_f16 v[20:23], v[238:241], v[210:213], v[20:23]
	v_mfma_f32_16x16x32_f16 v[104:107], v[238:241], v[218:221], v[104:107]
	v_mfma_f32_16x16x32_f16 v[108:111], v[242:245], v[210:213], v[108:111]
	v_mfma_f32_16x16x32_f16 v[112:115], v[242:245], v[214:217], v[112:115]
	v_mfma_f32_16x16x32_f16 v[116:119], v[242:245], v[218:221], v[116:119]
	v_mfma_f32_16x16x32_f16 v[230:233], v[238:241], v[214:217], v[230:233]
	v_mfma_f32_16x16x32_f16 v[234:237], v[238:241], v[222:225], v[234:237]
	v_mfma_f32_16x16x32_f16 v[226:229], v[242:245], v[222:225], v[226:229]
	s_setprio 0
	ds_read_b128 v[238:241], v130 offset:4096
	ds_read_b128 v[242:245], v130 offset:6144
	v_cvt_pk_f16_f32 v53, v58, v59
	v_cvt_pk_f16_f32 v52, v56, v57
	ds_write_b64 v100, v[52:53] offset:53248
	s_add_u32 s70, s22, 0xa0900
	s_addc_u32 s71, s90, 0
	s_add_u32 s100, s22, 0x80900
	s_addc_u32 s101, s90, 0
	global_load_dwordx4 v[48:51], v201, s[100:101] nt
	s_setprio 1
	s_waitcnt lgkmcnt(1)
	v_mfma_f32_16x16x32_f16 v[24:27], v[238:241], v[210:213], v[24:27]
	v_mfma_f32_16x16x32_f16 v[120:123], v[238:241], v[222:225], v[120:123]
	v_mfma_f32_16x16x32_f16 v[124:127], v[242:245], v[210:213], v[124:127]
	v_mfma_f32_16x16x32_f16 v[146:149], v[242:245], v[214:217], v[146:149]
	v_mfma_f32_16x16x32_f16 v[134:137], v[242:245], v[222:225], v[134:137]
	v_mfma_f32_16x16x32_f16 v[138:141], v[238:241], v[214:217], v[138:141]
	v_mfma_f32_16x16x32_f16 v[142:145], v[238:241], v[218:221], v[142:145]
	v_mfma_f32_16x16x32_f16 v[150:153], v[242:245], v[218:221], v[150:153]
	s_setprio 0
	ds_read_b128 v[238:241], v130 offset:8192
	ds_read_b128 v[242:245], v130 offset:10240
	v_cvt_pk_f16_f32 v57, v62, v63
	v_cvt_pk_f16_f32 v56, v60, v61
	ds_write_b64 v100, v[56:57] offset:57344
	s_add_u32 s70, s22, 0xc0900
	s_addc_u32 s71, s90, 0
	s_add_u32 s100, s22, 0xa0900
	s_addc_u32 s101, s90, 0
	global_load_dwordx4 v[52:55], v201, s[100:101] nt
	s_add_u32 s100, s22, 0xc0900
	s_addc_u32 s101, s90, 0
	global_load_dwordx4 v[56:59], v201, s[100:101] nt
	s_setprio 1
	s_waitcnt lgkmcnt(1)
	v_mfma_f32_16x16x32_f16 v[28:31], v[238:241], v[214:217], v[28:31]
	v_mfma_f32_16x16x32_f16 v[246:249], v[238:241], v[210:213], v[12:15]
	v_mfma_f32_16x16x32_f16 v[170:173], v[238:241], v[218:221], v[170:173]
	v_mfma_f32_16x16x32_f16 v[162:165], v[238:241], v[222:225], v[162:165]
	v_mfma_f32_16x16x32_f16 v[174:177], v[242:245], v[210:213], v[174:177]
	v_mfma_f32_16x16x32_f16 v[178:181], v[242:245], v[214:217], v[178:181]
	v_mfma_f32_16x16x32_f16 v[182:185], v[242:245], v[218:221], v[182:185]
	v_mfma_f32_16x16x32_f16 v[154:157], v[242:245], v[222:225], v[154:157]
	s_setprio 0
	ds_read_b128 v[12:15], v130 offset:12288
	ds_read_b128 v[238:241], v130 offset:14336
	v_cvt_pk_f16_f32 v39, v38, v39
	v_cvt_pk_f16_f32 v38, v36, v37
	ds_write_b64 v100, v[38:39] offset:61440
	s_add_u32 s70, s22, 0xe0900
	s_addc_u32 s71, s90, 0
	s_add_u32 s100, s22, 0xe0900
	s_addc_u32 s101, s90, 0
	global_load_dwordx4 v[60:63], v201, s[100:101] nt
	s_setprio 1
	s_waitcnt lgkmcnt(1)
	v_mfma_f32_16x16x32_f16 v[36:39], v[12:15], v[210:213], v[16:19]
	v_mfma_f32_16x16x32_f16 v[32:35], v[12:15], v[214:217], v[32:35]
	v_mfma_f32_16x16x32_f16 v[158:161], v[12:15], v[218:221], v[158:161]
	v_mfma_f32_16x16x32_f16 v[166:169], v[12:15], v[222:225], v[166:169]
	v_mfma_f32_16x16x32_f16 v[190:193], v[238:241], v[210:213], v[190:193]
	v_mfma_f32_16x16x32_f16 v[202:205], v[238:241], v[214:217], v[202:205]
	v_mfma_f32_16x16x32_f16 v[206:209], v[238:241], v[218:221], v[206:209]
	v_mfma_f32_16x16x32_f16 v[186:189], v[238:241], v[222:225], v[186:189]
	s_setprio 0
	s_waitcnt vmcnt(6)
	s_waitcnt lgkmcnt(0)
	s_barrier
	v_add_u32_e32 v250, 0x20000, v129
	v_add_u32_e32 v251, 0x20000, v130
	ds_read_b128 v[210:213], v131 offset:32768
	ds_read_b128 v[214:217], v131 offset:34816
	ds_read_b128 v[218:221], v131 offset:36864
	ds_read_b128 v[222:225], v131 offset:38912
	ds_read_b128 v[12:15], v250
	ds_read_b128 v[16:19], v250 offset:2048
	s_add_u32 s70, s22, 0xa00
	v_lshl_add_u64 v[92:93], s[42:43], 0, v[196:197]
	s_addc_u32 s71, s90, 0
	s_mov_b32 m0, s1
	v_cvt_pk_f16_f32 v3, v2, v3
	global_load_lds_dwordx4 v[92:93], off
	v_cvt_pk_f16_f32 v2, v0, v1
	ds_write_b64 v100, v[2:3]
	s_setprio 1
	s_waitcnt lgkmcnt(1)
	v_mfma_f32_16x16x32_f16 v[104:107], v[12:15], v[218:221], v[104:107]
	v_mfma_f32_16x16x32_f16 v[108:111], v[16:19], v[210:213], v[108:111]
	v_mfma_f32_16x16x32_f16 v[112:115], v[16:19], v[214:217], v[112:115]
	v_mfma_f32_16x16x32_f16 v[116:119], v[16:19], v[218:221], v[116:119]
	v_mfma_f32_16x16x32_f16 v[238:241], v[12:15], v[210:213], v[20:23]
	v_mfma_f32_16x16x32_f16 v[230:233], v[12:15], v[214:217], v[230:233]
	v_mfma_f32_16x16x32_f16 v[234:237], v[12:15], v[222:225], v[234:237]
	v_mfma_f32_16x16x32_f16 v[226:229], v[16:19], v[222:225], v[226:229]
	s_setprio 0
	ds_read_b128 v[16:19], v250 offset:4096
	ds_read_b128 v[20:23], v250 offset:6144
	s_mov_b32 m0, s92
	v_lshl_add_u64 v[12:13], v[92:93], 0, s[58:59]
	global_load_lds_dwordx4 v[12:13], off
	v_cvt_pk_f16_f32 v13, v66, v67
	v_cvt_pk_f16_f32 v12, v64, v65
	ds_write_b64 v100, v[12:13] offset:4096
	s_add_u32 s0, s22, 0x20a00
	s_addc_u32 s1, s90, 0
	s_add_u32 s100, s22, 0xa00
	s_addc_u32 s101, s90, 0
	global_load_dwordx4 v[0:3], v201, s[100:101] nt
	s_setprio 1
	s_waitcnt lgkmcnt(1)
	v_mfma_f32_16x16x32_f16 v[64:67], v[16:19], v[210:213], v[24:27]
	v_mfma_f32_16x16x32_f16 v[120:123], v[16:19], v[222:225], v[120:123]
	v_mfma_f32_16x16x32_f16 v[124:127], v[20:23], v[210:213], v[124:127]
	v_mfma_f32_16x16x32_f16 v[146:149], v[20:23], v[214:217], v[146:149]
	v_mfma_f32_16x16x32_f16 v[134:137], v[20:23], v[222:225], v[134:137]
	v_mfma_f32_16x16x32_f16 v[138:141], v[16:19], v[214:217], v[138:141]
	v_mfma_f32_16x16x32_f16 v[142:145], v[16:19], v[218:221], v[142:145]
	v_mfma_f32_16x16x32_f16 v[150:153], v[20:23], v[218:221], v[150:153]
	s_setprio 0
	ds_read_b128 v[20:23], v250 offset:8192
	ds_read_b128 v[24:27], v250 offset:10240
	s_mov_b32 m0, s91
	v_lshl_add_u64 v[16:17], v[92:93], 0, s[60:61]
	global_load_lds_dwordx4 v[16:17], off
	v_cvt_pk_f16_f32 v17, v70, v71
	v_cvt_pk_f16_f32 v16, v68, v69
	ds_write_b64 v100, v[16:17] offset:8192
	s_add_u32 s0, s22, 0x40a00
	s_addc_u32 s1, s90, 0
	s_add_u32 s100, s22, 0x20a00
	s_addc_u32 s101, s90, 0
	global_load_dwordx4 v[12:15], v201, s[100:101] nt
	s_setprio 1
	s_waitcnt lgkmcnt(1)
	v_mfma_f32_16x16x32_f16 v[68:71], v[20:23], v[210:213], v[246:249]
	v_mfma_f32_16x16x32_f16 v[242:245], v[20:23], v[214:217], v[28:31]
	v_mfma_f32_16x16x32_f16 v[170:173], v[20:23], v[218:221], v[170:173]
	v_mfma_f32_16x16x32_f16 v[162:165], v[20:23], v[222:225], v[162:165]
	v_mfma_f32_16x16x32_f16 v[174:177], v[24:27], v[210:213], v[174:177]
	v_mfma_f32_16x16x32_f16 v[178:181], v[24:27], v[214:217], v[178:181]
	v_mfma_f32_16x16x32_f16 v[182:185], v[24:27], v[218:221], v[182:185]
	v_mfma_f32_16x16x32_f16 v[154:157], v[24:27], v[222:225], v[154:157]
	s_setprio 0
	ds_read_b128 v[24:27], v250 offset:12288
	ds_read_b128 v[28:31], v250 offset:14336
	s_mov_b32 m0, s73
	v_lshl_add_u64 v[20:21], v[92:93], 0, s[62:63]
	global_load_lds_dwordx4 v[20:21], off
	v_cvt_pk_f16_f32 v21, v74, v75
	v_cvt_pk_f16_f32 v20, v72, v73
	ds_write_b64 v100, v[20:21] offset:12288
	s_add_u32 s0, s22, 0x60a00
	s_addc_u32 s1, s90, 0
	s_add_u32 s100, s22, 0x40a00
	s_addc_u32 s101, s90, 0
	global_load_dwordx4 v[16:19], v201, s[100:101] nt
	s_setprio 1
	s_waitcnt lgkmcnt(1)
	v_mfma_f32_16x16x32_f16 v[72:75], v[24:27], v[210:213], v[36:39]
	v_mfma_f32_16x16x32_f16 v[246:249], v[24:27], v[214:217], v[32:35]
	v_mfma_f32_16x16x32_f16 v[158:161], v[24:27], v[218:221], v[158:161]
	v_mfma_f32_16x16x32_f16 v[166:169], v[24:27], v[222:225], v[166:169]
	v_mfma_f32_16x16x32_f16 v[190:193], v[28:31], v[210:213], v[190:193]
	v_mfma_f32_16x16x32_f16 v[202:205], v[28:31], v[214:217], v[202:205]
	v_mfma_f32_16x16x32_f16 v[206:209], v[28:31], v[218:221], v[206:209]
	v_mfma_f32_16x16x32_f16 v[186:189], v[28:31], v[222:225], v[186:189]
	s_setprio 0
	ds_read_b128 v[210:213], v128 offset:32768
	ds_read_b128 v[214:217], v128 offset:34816
	ds_read_b128 v[218:221], v128 offset:36864
	ds_read_b128 v[222:225], v128 offset:38912
	ds_read_b128 v[28:31], v251
	ds_read_b128 v[32:35], v251 offset:2048
	v_cvt_pk_f16_f32 v25, v78, v79
	v_cvt_pk_f16_f32 v24, v76, v77
	ds_write_b64 v100, v[24:25] offset:16384
	s_add_u32 s0, s22, 0x80a00
	s_addc_u32 s1, s90, 0
	s_add_u32 s100, s22, 0x60a00
	s_addc_u32 s101, s90, 0
	global_load_dwordx4 v[20:23], v201, s[100:101] nt
	s_setprio 1
	s_waitcnt lgkmcnt(1)
	v_mfma_f32_16x16x32_f16 v[76:79], v[28:31], v[210:213], v[238:241]
	v_mfma_f32_16x16x32_f16 v[104:107], v[28:31], v[218:221], v[104:107]
	v_mfma_f32_16x16x32_f16 v[108:111], v[32:35], v[210:213], v[108:111]
	v_mfma_f32_16x16x32_f16 v[112:115], v[32:35], v[214:217], v[112:115]
	v_mfma_f32_16x16x32_f16 v[116:119], v[32:35], v[218:221], v[116:119]
	v_mfma_f32_16x16x32_f16 v[230:233], v[28:31], v[214:217], v[230:233]
	v_mfma_f32_16x16x32_f16 v[234:237], v[28:31], v[222:225], v[234:237]
	v_mfma_f32_16x16x32_f16 v[226:229], v[32:35], v[222:225], v[226:229]
	s_setprio 0
	ds_read_b128 v[32:35], v251 offset:4096
	ds_read_b128 v[36:39], v251 offset:6144
	v_cvt_pk_f16_f32 v29, v82, v83
	v_cvt_pk_f16_f32 v28, v80, v81
	ds_write_b64 v100, v[28:29] offset:20480
	s_add_u32 s0, s22, 0xa0a00
	s_addc_u32 s1, s90, 0
	s_add_u32 s100, s22, 0x80a00
	s_addc_u32 s101, s90, 0
	global_load_dwordx4 v[24:27], v201, s[100:101] nt
	s_setprio 1
	s_waitcnt lgkmcnt(1)
	v_mfma_f32_16x16x32_f16 v[80:83], v[32:35], v[210:213], v[64:67]
	v_mfma_f32_16x16x32_f16 v[120:123], v[32:35], v[222:225], v[120:123]
	v_mfma_f32_16x16x32_f16 v[124:127], v[36:39], v[210:213], v[124:127]
	v_mfma_f32_16x16x32_f16 v[146:149], v[36:39], v[214:217], v[146:149]
	v_mfma_f32_16x16x32_f16 v[134:137], v[36:39], v[222:225], v[134:137]
	v_mfma_f32_16x16x32_f16 v[138:141], v[32:35], v[214:217], v[138:141]
	v_mfma_f32_16x16x32_f16 v[142:145], v[32:35], v[218:221], v[142:145]
	v_mfma_f32_16x16x32_f16 v[150:153], v[36:39], v[218:221], v[150:153]
	s_setprio 0
	ds_read_b128 v[36:39], v251 offset:8192
	ds_read_b128 v[64:67], v251 offset:10240
	v_cvt_pk_f16_f32 v33, v86, v87
	v_cvt_pk_f16_f32 v32, v84, v85
	ds_write_b64 v100, v[32:33] offset:24576
	s_add_u32 s0, s22, 0xc0a00
	s_addc_u32 s1, s90, 0
	s_add_u32 s100, s22, 0xa0a00
	s_addc_u32 s101, s90, 0
	global_load_dwordx4 v[28:31], v201, s[100:101] nt
	s_add_u32 s100, s22, 0xc0a00
	s_addc_u32 s101, s90, 0
	global_load_dwordx4 v[32:35], v201, s[100:101] nt
	s_setprio 1
	s_waitcnt lgkmcnt(1)
	v_mfma_f32_16x16x32_f16 v[68:71], v[36:39], v[210:213], v[68:71]
	v_mfma_f32_16x16x32_f16 v[84:87], v[36:39], v[214:217], v[242:245]
	v_mfma_f32_16x16x32_f16 v[170:173], v[36:39], v[218:221], v[170:173]
	v_mfma_f32_16x16x32_f16 v[162:165], v[36:39], v[222:225], v[162:165]
	v_mfma_f32_16x16x32_f16 v[174:177], v[64:67], v[210:213], v[174:177]
	v_mfma_f32_16x16x32_f16 v[178:181], v[64:67], v[214:217], v[178:181]
	v_mfma_f32_16x16x32_f16 v[182:185], v[64:67], v[218:221], v[182:185]
	v_mfma_f32_16x16x32_f16 v[154:157], v[64:67], v[222:225], v[154:157]
	s_setprio 0
	ds_read_b128 v[64:67], v251 offset:12288
	ds_read_b128 v[238:241], v251 offset:14336
	v_cvt_pk_f16_f32 v37, v90, v91
	v_cvt_pk_f16_f32 v36, v88, v89
	ds_write_b64 v100, v[36:37] offset:28672
	s_add_u32 s0, s22, 0xe0a00
	s_addc_u32 s1, s90, 0
	s_add_u32 s100, s22, 0xe0a00
	s_addc_u32 s101, s90, 0
	global_load_dwordx4 v[36:39], v201, s[100:101] nt
	s_setprio 1
	s_waitcnt lgkmcnt(1)
	v_mfma_f32_16x16x32_f16 v[72:75], v[64:67], v[210:213], v[72:75]
	v_mfma_f32_16x16x32_f16 v[88:91], v[64:67], v[214:217], v[246:249]
	v_mfma_f32_16x16x32_f16 v[158:161], v[64:67], v[218:221], v[158:161]
	v_mfma_f32_16x16x32_f16 v[166:169], v[64:67], v[222:225], v[166:169]
	v_mfma_f32_16x16x32_f16 v[190:193], v[238:241], v[210:213], v[190:193]
	v_mfma_f32_16x16x32_f16 v[202:205], v[238:241], v[214:217], v[202:205]
	v_mfma_f32_16x16x32_f16 v[206:209], v[238:241], v[218:221], v[206:209]
	v_mfma_f32_16x16x32_f16 v[186:189], v[238:241], v[222:225], v[186:189]
	s_setprio 0
	s_waitcnt vmcnt(6)
	s_waitcnt lgkmcnt(0)
	s_barrier
	ds_read_b128 v[210:213], v131
	ds_read_b128 v[214:217], v131 offset:2048
	ds_read_b128 v[218:221], v131 offset:4096
	ds_read_b128 v[222:225], v131 offset:6144
	ds_read_b128 v[64:67], v129
	ds_read_b128 v[238:241], v129 offset:2048
	s_add_u32 s70, s22, 0xb00
	v_lshl_add_u64 v[92:93], s[44:45], 0, v[196:197]
	s_addc_u32 s71, s90, 0
	v_readfirstlane_b32 s0, v95
	s_mov_b32 m0, s0
	v_cvt_pk_f16_f32 v7, v6, v7
	global_load_lds_dwordx4 v[92:93], off
	v_cvt_pk_f16_f32 v6, v4, v5
	ds_write_b64 v100, v[6:7] offset:32768
	s_setprio 1
	s_waitcnt lgkmcnt(1)
	v_mfma_f32_16x16x32_f16 v[76:79], v[64:67], v[210:213], v[76:79]
	v_mfma_f32_16x16x32_f16 v[104:107], v[64:67], v[218:221], v[104:107]
	v_mfma_f32_16x16x32_f16 v[108:111], v[238:241], v[210:213], v[108:111]
	v_mfma_f32_16x16x32_f16 v[112:115], v[238:241], v[214:217], v[112:115]
	v_mfma_f32_16x16x32_f16 v[116:119], v[238:241], v[218:221], v[116:119]
	v_mfma_f32_16x16x32_f16 v[230:233], v[64:67], v[214:217], v[230:233]
	v_mfma_f32_16x16x32_f16 v[234:237], v[64:67], v[222:225], v[234:237]
	v_mfma_f32_16x16x32_f16 v[226:229], v[238:241], v[222:225], v[226:229]
	s_setprio 0
	ds_read_b128 v[238:241], v129 offset:4096
	ds_read_b128 v[242:245], v129 offset:6144
	v_readfirstlane_b32 s72, v96
	v_lshl_add_u64 v[64:65], v[92:93], 0, s[58:59]
	s_mov_b32 m0, s72
	v_cvt_pk_f16_f32 v11, v10, v11
	global_load_lds_dwordx4 v[64:65], off
	v_cvt_pk_f16_f32 v10, v8, v9
	ds_write_b64 v100, v[10:11] offset:36864
	s_add_u32 s70, s22, 0x20b00
	s_addc_u32 s71, s90, 0
	s_add_u32 s100, s22, 0xb00
	s_addc_u32 s101, s90, 0
	global_load_dwordx4 v[4:7], v201, s[100:101] nt
	s_setprio 1
	s_waitcnt lgkmcnt(1)
	v_mfma_f32_16x16x32_f16 v[8:11], v[238:241], v[210:213], v[80:83]
	v_mfma_f32_16x16x32_f16 v[80:83], v[238:241], v[214:217], v[138:141]
	v_mfma_f32_16x16x32_f16 v[138:141], v[238:241], v[218:221], v[142:145]
	v_mfma_f32_16x16x32_f16 v[120:123], v[238:241], v[222:225], v[120:123]
	v_mfma_f32_16x16x32_f16 v[124:127], v[242:245], v[210:213], v[124:127]
	v_mfma_f32_16x16x32_f16 v[142:145], v[242:245], v[214:217], v[146:149]
	v_mfma_f32_16x16x32_f16 v[146:149], v[242:245], v[218:221], v[150:153]
	v_mfma_f32_16x16x32_f16 v[134:137], v[242:245], v[222:225], v[134:137]
	s_setprio 0
	s_nop 0
	ds_read_b128 v[150:153], v129 offset:8192
	ds_read_b128 v[238:241], v129 offset:10240
	v_readfirstlane_b32 s71, v97
	v_lshl_add_u64 v[198:199], v[92:93], 0, s[60:61]
	s_mov_b32 m0, s71
	v_cvt_pk_f16_f32 v43, v42, v43
	global_load_lds_dwordx4 v[198:199], off
	v_cvt_pk_f16_f32 v42, v40, v41
	ds_write_b64 v100, v[42:43] offset:40960
	s_add_u32 s80, s22, 0x40b00
	s_addc_u32 s81, s90, 0
	s_add_u32 s100, s22, 0x20b00
	s_addc_u32 s101, s90, 0
	global_load_dwordx4 v[64:67], v201, s[100:101] nt
	s_setprio 1
	s_waitcnt lgkmcnt(1)
	v_mfma_f32_16x16x32_f16 v[68:71], v[150:153], v[210:213], v[68:71]
	v_mfma_f32_16x16x32_f16 v[84:87], v[150:153], v[214:217], v[84:87]
	v_mfma_f32_16x16x32_f16 v[170:173], v[150:153], v[218:221], v[170:173]
	v_mfma_f32_16x16x32_f16 v[150:153], v[150:153], v[222:225], v[162:165]
	v_mfma_f32_16x16x32_f16 v[162:165], v[238:241], v[210:213], v[174:177]
	v_mfma_f32_16x16x32_f16 v[174:177], v[238:241], v[214:217], v[178:181]
	v_mfma_f32_16x16x32_f16 v[178:181], v[238:241], v[218:221], v[182:185]
	v_mfma_f32_16x16x32_f16 v[154:157], v[238:241], v[222:225], v[154:157]
	s_setprio 0
	s_nop 0
	ds_read_b128 v[182:185], v129 offset:12288
	ds_read_b128 v[238:241], v129 offset:14336
	v_readfirstlane_b32 s70, v98
	v_lshl_add_u64 v[92:93], v[92:93], 0, s[62:63]
	s_mov_b32 m0, s70
	v_cvt_pk_f16_f32 v47, v46, v47
	global_load_lds_dwordx4 v[92:93], off
	v_cvt_pk_f16_f32 v46, v44, v45
	ds_write_b64 v100, v[46:47] offset:45056
	s_add_u32 s80, s22, 0x60b00
	s_addc_u32 s81, s90, 0
	s_add_u32 s100, s22, 0x40b00
	s_addc_u32 s101, s90, 0
	global_load_dwordx4 v[40:43], v201, s[100:101] nt
	s_setprio 1
	s_waitcnt lgkmcnt(1)
	v_mfma_f32_16x16x32_f16 v[72:75], v[182:185], v[210:213], v[72:75]
	v_mfma_f32_16x16x32_f16 v[88:91], v[182:185], v[214:217], v[88:91]
	v_mfma_f32_16x16x32_f16 v[158:161], v[182:185], v[218:221], v[158:161]
	v_mfma_f32_16x16x32_f16 v[166:169], v[182:185], v[222:225], v[166:169]
	v_mfma_f32_16x16x32_f16 v[182:185], v[238:241], v[210:213], v[190:193]
	v_mfma_f32_16x16x32_f16 v[190:193], v[238:241], v[214:217], v[202:205]
	v_mfma_f32_16x16x32_f16 v[202:205], v[238:241], v[218:221], v[206:209]
	v_mfma_f32_16x16x32_f16 v[186:189], v[238:241], v[222:225], v[186:189]
	s_setprio 0
	s_nop 0
	ds_read_b128 v[206:209], v128
	ds_read_b128 v[210:213], v128 offset:2048
	ds_read_b128 v[214:217], v128 offset:4096
	ds_read_b128 v[218:221], v128 offset:6144
	ds_read_b128 v[222:225], v130
	ds_read_b128 v[238:241], v130 offset:2048
	v_cvt_pk_f16_f32 v51, v50, v51
	v_cvt_pk_f16_f32 v50, v48, v49
	ds_write_b64 v100, v[50:51] offset:49152
	s_add_u32 s80, s22, 0x80b00
	s_addc_u32 s81, s90, 0
	s_add_u32 s100, s22, 0x60b00
	s_addc_u32 s101, s90, 0
	global_load_dwordx4 v[44:47], v201, s[100:101] nt
	s_setprio 1
	s_waitcnt lgkmcnt(1)
	v_mfma_f32_16x16x32_f16 v[76:79], v[222:225], v[206:209], v[76:79]
	v_mfma_f32_16x16x32_f16 v[104:107], v[222:225], v[214:217], v[104:107]
	v_mfma_f32_16x16x32_f16 v[108:111], v[238:241], v[206:209], v[108:111]
	v_mfma_f32_16x16x32_f16 v[112:115], v[238:241], v[210:213], v[112:115]
	v_mfma_f32_16x16x32_f16 v[116:119], v[238:241], v[214:217], v[116:119]
	v_mfma_f32_16x16x32_f16 v[230:233], v[222:225], v[210:213], v[230:233]
	v_mfma_f32_16x16x32_f16 v[222:225], v[222:225], v[218:221], v[234:237]
	v_mfma_f32_16x16x32_f16 v[226:229], v[238:241], v[218:221], v[226:229]
	s_setprio 0
	s_nop 0
	ds_read_b128 v[234:237], v130 offset:4096
	ds_read_b128 v[238:241], v130 offset:6144
	v_cvt_pk_f16_f32 v55, v54, v55
	v_cvt_pk_f16_f32 v54, v52, v53
	ds_write_b64 v100, v[54:55] offset:53248
	s_add_u32 s80, s22, 0xa0b00
	s_addc_u32 s81, s90, 0
	s_add_u32 s100, s22, 0x80b00
	s_addc_u32 s101, s90, 0
	global_load_dwordx4 v[48:51], v201, s[100:101] nt
	s_setprio 1
	s_waitcnt lgkmcnt(1)
	v_mfma_f32_16x16x32_f16 v[80:83], v[234:237], v[210:213], v[80:83]
	v_mfma_f32_16x16x32_f16 v[120:123], v[234:237], v[218:221], v[120:123]
	v_mfma_f32_16x16x32_f16 v[124:127], v[238:241], v[206:209], v[124:127]
	v_mfma_f32_16x16x32_f16 v[146:149], v[238:241], v[214:217], v[146:149]
	v_mfma_f32_16x16x32_f16 v[134:137], v[238:241], v[218:221], v[134:137]
	v_mfma_f32_16x16x32_f16 v[242:245], v[234:237], v[206:209], v[8:11]
	v_mfma_f32_16x16x32_f16 v[138:141], v[234:237], v[214:217], v[138:141]
	v_mfma_f32_16x16x32_f16 v[142:145], v[238:241], v[210:213], v[142:145]
	s_setprio 0
	ds_read_b128 v[8:11], v130 offset:8192
	ds_read_b128 v[234:237], v130 offset:10240
	v_cvt_pk_f16_f32 v59, v58, v59
	v_cvt_pk_f16_f32 v58, v56, v57
	ds_write_b64 v100, v[58:59] offset:57344
	s_add_u32 s80, s22, 0xc0b00
	s_addc_u32 s81, s90, 0
	s_add_u32 s100, s22, 0xa0b00
	s_addc_u32 s101, s90, 0
	global_load_dwordx4 v[52:55], v201, s[100:101] nt
	s_add_u32 s100, s22, 0xc0b00
	s_addc_u32 s101, s90, 0
	global_load_dwordx4 v[56:59], v201, s[100:101] nt
	s_setprio 1
	s_waitcnt lgkmcnt(1)
	v_mfma_f32_16x16x32_f16 v[84:87], v[8:11], v[210:213], v[84:87]
	v_mfma_f32_16x16x32_f16 v[238:241], v[8:11], v[206:209], v[68:71]
	v_mfma_f32_16x16x32_f16 v[170:173], v[8:11], v[214:217], v[170:173]
	v_mfma_f32_16x16x32_f16 v[150:153], v[8:11], v[218:221], v[150:153]
	v_mfma_f32_16x16x32_f16 v[162:165], v[234:237], v[206:209], v[162:165]
	v_mfma_f32_16x16x32_f16 v[174:177], v[234:237], v[210:213], v[174:177]
	v_mfma_f32_16x16x32_f16 v[178:181], v[234:237], v[214:217], v[178:181]
	v_mfma_f32_16x16x32_f16 v[154:157], v[234:237], v[218:221], v[154:157]
	s_setprio 0
	ds_read_b128 v[8:11], v130 offset:12288
	ds_read_b128 v[68:71], v130 offset:14336
	v_cvt_pk_f16_f32 v63, v62, v63
	v_cvt_pk_f16_f32 v62, v60, v61
	ds_write_b64 v100, v[62:63] offset:61440
	s_add_u32 s80, s22, 0xe0b00
	s_addc_u32 s81, s90, 0
	s_add_u32 s100, s22, 0xe0b00
	s_addc_u32 s101, s90, 0
	global_load_dwordx4 v[60:63], v201, s[100:101] nt
	s_setprio 1
	s_waitcnt lgkmcnt(1)
	v_mfma_f32_16x16x32_f16 v[88:91], v[8:11], v[210:213], v[88:91]
	v_mfma_f32_16x16x32_f16 v[234:237], v[8:11], v[206:209], v[72:75]
	v_mfma_f32_16x16x32_f16 v[158:161], v[8:11], v[214:217], v[158:161]
	v_mfma_f32_16x16x32_f16 v[166:169], v[8:11], v[218:221], v[166:169]
	v_mfma_f32_16x16x32_f16 v[182:185], v[68:71], v[206:209], v[182:185]
	v_mfma_f32_16x16x32_f16 v[190:193], v[68:71], v[210:213], v[190:193]
	v_mfma_f32_16x16x32_f16 v[202:205], v[68:71], v[214:217], v[202:205]
	v_mfma_f32_16x16x32_f16 v[186:189], v[68:71], v[218:221], v[186:189]
	s_setprio 0
	s_waitcnt vmcnt(6)
	s_waitcnt lgkmcnt(0)
	s_barrier
	ds_read_b128 v[206:209], v131 offset:32768
	ds_read_b128 v[210:213], v131 offset:34816
	ds_read_b128 v[214:217], v131 offset:36864
	ds_read_b128 v[218:221], v131 offset:38912
	ds_read_b128 v[68:71], v129 offset:32768
	ds_read_b128 v[72:75], v129 offset:34816
	s_add_u32 s80, s22, 0xc00
	v_lshl_add_u64 v[92:93], s[46:47], 0, v[196:197]
	s_addc_u32 s81, s90, 0
	v_readfirstlane_b32 s1, v94
	s_mov_b32 m0, s1
	v_cvt_pk_f16_f32 v3, v2, v3
	global_load_lds_dwordx4 v[92:93], off
	v_cvt_pk_f16_f32 v2, v0, v1
	ds_write_b64 v100, v[2:3]
	s_setprio 1
	s_waitcnt lgkmcnt(1)
	v_mfma_f32_16x16x32_f16 v[0:3], v[68:71], v[206:209], v[76:79]
	v_mfma_f32_16x16x32_f16 v[104:107], v[68:71], v[214:217], v[104:107]
	v_mfma_f32_16x16x32_f16 v[108:111], v[72:75], v[206:209], v[108:111]
	v_mfma_f32_16x16x32_f16 v[112:115], v[72:75], v[210:213], v[112:115]
	v_mfma_f32_16x16x32_f16 v[116:119], v[72:75], v[214:217], v[116:119]
	v_mfma_f32_16x16x32_f16 v[230:233], v[68:71], v[210:213], v[230:233]
	v_mfma_f32_16x16x32_f16 v[222:225], v[68:71], v[218:221], v[222:225]
	v_mfma_f32_16x16x32_f16 v[226:229], v[72:75], v[218:221], v[226:229]
	s_setprio 0
	ds_read_b128 v[72:75], v129 offset:36864
	ds_read_b128 v[76:79], v129 offset:38912
	v_readfirstlane_b32 s92, v99
	v_lshl_add_u64 v[68:69], v[92:93], 0, s[58:59]
	s_mov_b32 m0, s92
	v_cvt_pk_f16_f32 v15, v14, v15
	global_load_lds_dwordx4 v[68:69], off
	v_cvt_pk_f16_f32 v14, v12, v13
	ds_write_b64 v100, v[14:15] offset:4096
	s_add_u32 s80, s22, 0x20c00
	s_addc_u32 s81, s90, 0
	s_add_u32 s100, s22, 0xc00
	s_addc_u32 s101, s90, 0
	global_load_dwordx4 v[8:11], v201, s[100:101] nt
	s_setprio 1
	s_waitcnt lgkmcnt(1)
	v_mfma_f32_16x16x32_f16 v[12:15], v[72:75], v[206:209], v[242:245]
	v_mfma_f32_16x16x32_f16 v[120:123], v[72:75], v[218:221], v[120:123]
	v_mfma_f32_16x16x32_f16 v[124:127], v[76:79], v[206:209], v[124:127]
	v_mfma_f32_16x16x32_f16 v[146:149], v[76:79], v[214:217], v[146:149]
	v_mfma_f32_16x16x32_f16 v[134:137], v[76:79], v[218:221], v[134:137]
	v_mfma_f32_16x16x32_f16 v[242:245], v[72:75], v[210:213], v[80:83]
	v_mfma_f32_16x16x32_f16 v[138:141], v[72:75], v[214:217], v[138:141]
	v_mfma_f32_16x16x32_f16 v[142:145], v[76:79], v[210:213], v[142:145]
	s_setprio 0
	ds_read_b128 v[76:79], v129 offset:40960
	ds_read_b128 v[80:83], v129 offset:43008
	v_readfirstlane_b32 s91, v101
	v_lshl_add_u64 v[72:73], v[92:93], 0, s[60:61]
	s_mov_b32 m0, s91
	v_cvt_pk_f16_f32 v19, v18, v19
	global_load_lds_dwordx4 v[72:73], off
	v_cvt_pk_f16_f32 v18, v16, v17
	ds_write_b64 v100, v[18:19] offset:8192
	s_add_u32 s80, s22, 0x40c00
	s_addc_u32 s81, s90, 0
	s_add_u32 s100, s22, 0x20c00
	s_addc_u32 s101, s90, 0
	global_load_dwordx4 v[68:71], v201, s[100:101] nt
	s_setprio 1
	s_waitcnt lgkmcnt(1)
	v_mfma_f32_16x16x32_f16 v[16:19], v[76:79], v[206:209], v[238:241]
	v_mfma_f32_16x16x32_f16 v[238:241], v[76:79], v[210:213], v[84:87]
	v_mfma_f32_16x16x32_f16 v[170:173], v[76:79], v[214:217], v[170:173]
	v_mfma_f32_16x16x32_f16 v[150:153], v[76:79], v[218:221], v[150:153]
	v_mfma_f32_16x16x32_f16 v[162:165], v[80:83], v[206:209], v[162:165]
	v_mfma_f32_16x16x32_f16 v[174:177], v[80:83], v[210:213], v[174:177]
	v_mfma_f32_16x16x32_f16 v[178:181], v[80:83], v[214:217], v[178:181]
	v_mfma_f32_16x16x32_f16 v[154:157], v[80:83], v[218:221], v[154:157]
	s_setprio 0
	ds_read_b128 v[80:83], v129 offset:45056
	ds_read_b128 v[84:87], v129 offset:47104
	v_readfirstlane_b32 s73, v102
	v_lshl_add_u64 v[76:77], v[92:93], 0, s[62:63]
	s_mov_b32 m0, s73
	v_cvt_pk_f16_f32 v23, v22, v23
	global_load_lds_dwordx4 v[76:77], off
	v_cvt_pk_f16_f32 v22, v20, v21
	ds_write_b64 v100, v[22:23] offset:12288
	s_add_u32 s80, s22, 0x60c00
	s_addc_u32 s81, s90, 0
	s_add_u32 s100, s22, 0x40c00
	s_addc_u32 s101, s90, 0
	global_load_dwordx4 v[72:75], v201, s[100:101] nt
	s_setprio 1
	s_waitcnt lgkmcnt(1)
	v_mfma_f32_16x16x32_f16 v[20:23], v[80:83], v[206:209], v[234:237]
	v_mfma_f32_16x16x32_f16 v[234:237], v[80:83], v[210:213], v[88:91]
	v_mfma_f32_16x16x32_f16 v[158:161], v[80:83], v[214:217], v[158:161]
	v_mfma_f32_16x16x32_f16 v[166:169], v[80:83], v[218:221], v[166:169]
	v_mfma_f32_16x16x32_f16 v[182:185], v[84:87], v[206:209], v[182:185]
	v_mfma_f32_16x16x32_f16 v[190:193], v[84:87], v[210:213], v[190:193]
	v_mfma_f32_16x16x32_f16 v[202:205], v[84:87], v[214:217], v[202:205]
	v_mfma_f32_16x16x32_f16 v[186:189], v[84:87], v[218:221], v[186:189]
	s_setprio 0
	ds_read_b128 v[206:209], v128 offset:32768
	ds_read_b128 v[210:213], v128 offset:34816
	ds_read_b128 v[214:217], v128 offset:36864
	ds_read_b128 v[218:221], v128 offset:38912
	ds_read_b128 v[84:87], v130 offset:32768
	ds_read_b128 v[88:91], v130 offset:34816
	v_cvt_pk_f16_f32 v27, v26, v27
	v_cvt_pk_f16_f32 v26, v24, v25
	ds_write_b64 v100, v[26:27] offset:16384
	s_add_u32 s80, s22, 0x80c00
	s_addc_u32 s81, s90, 0
	s_add_u32 s100, s22, 0x60c00
	s_addc_u32 s101, s90, 0
	global_load_dwordx4 v[76:79], v201, s[100:101] nt
	s_setprio 1
	s_waitcnt lgkmcnt(1)
	v_mfma_f32_16x16x32_f16 v[24:27], v[84:87], v[206:209], v[0:3]
	v_mfma_f32_16x16x32_f16 v[104:107], v[84:87], v[214:217], v[104:107]
	v_mfma_f32_16x16x32_f16 v[108:111], v[88:91], v[206:209], v[108:111]
	v_mfma_f32_16x16x32_f16 v[112:115], v[88:91], v[210:213], v[112:115]
	v_mfma_f32_16x16x32_f16 v[116:119], v[88:91], v[214:217], v[116:119]
	v_mfma_f32_16x16x32_f16 v[230:233], v[84:87], v[210:213], v[230:233]
	v_mfma_f32_16x16x32_f16 v[222:225], v[84:87], v[218:221], v[222:225]
	v_mfma_f32_16x16x32_f16 v[226:229], v[88:91], v[218:221], v[226:229]
	s_setprio 0
	ds_read_b128 v[0:3], v130 offset:36864
	ds_read_b128 v[88:91], v130 offset:38912
	v_cvt_pk_f16_f32 v31, v30, v31
	v_cvt_pk_f16_f32 v30, v28, v29
	ds_write_b64 v100, v[30:31] offset:20480
	s_add_u32 s80, s22, 0xa0c00
	s_addc_u32 s81, s90, 0
	s_add_u32 s100, s22, 0x80c00
	s_addc_u32 s101, s90, 0
	global_load_dwordx4 v[80:83], v201, s[100:101] nt
	s_setprio 1
	s_waitcnt lgkmcnt(1)
	v_mfma_f32_16x16x32_f16 v[12:15], v[0:3], v[206:209], v[12:15]
	v_mfma_f32_16x16x32_f16 v[28:31], v[0:3], v[210:213], v[242:245]
	v_mfma_f32_16x16x32_f16 v[120:123], v[0:3], v[218:221], v[120:123]
	v_mfma_f32_16x16x32_f16 v[124:127], v[88:91], v[206:209], v[124:127]
	v_mfma_f32_16x16x32_f16 v[146:149], v[88:91], v[214:217], v[146:149]
	v_mfma_f32_16x16x32_f16 v[134:137], v[88:91], v[218:221], v[134:137]
	v_mfma_f32_16x16x32_f16 v[138:141], v[0:3], v[214:217], v[138:141]
	v_mfma_f32_16x16x32_f16 v[142:145], v[88:91], v[210:213], v[142:145]
	s_setprio 0
	ds_read_b128 v[0:3], v130 offset:40960
	ds_read_b128 v[242:245], v130 offset:43008
	v_cvt_pk_f16_f32 v35, v34, v35
	v_cvt_pk_f16_f32 v34, v32, v33
	ds_write_b64 v100, v[34:35] offset:24576
	s_add_u32 s80, s22, 0xc0c00
	s_addc_u32 s81, s90, 0
	s_add_u32 s100, s22, 0xa0c00
	s_addc_u32 s101, s90, 0
	global_load_dwordx4 v[84:87], v201, s[100:101] nt
	s_add_u32 s100, s22, 0xc0c00
	s_addc_u32 s101, s90, 0
	global_load_dwordx4 v[88:91], v201, s[100:101] nt
	s_setprio 1
	s_waitcnt lgkmcnt(1)
	v_mfma_f32_16x16x32_f16 v[16:19], v[0:3], v[206:209], v[16:19]
	v_mfma_f32_16x16x32_f16 v[32:35], v[0:3], v[210:213], v[238:241]
	v_mfma_f32_16x16x32_f16 v[170:173], v[0:3], v[214:217], v[170:173]
	v_mfma_f32_16x16x32_f16 v[150:153], v[0:3], v[218:221], v[150:153]
	v_mfma_f32_16x16x32_f16 v[162:165], v[242:245], v[206:209], v[162:165]
	v_mfma_f32_16x16x32_f16 v[174:177], v[242:245], v[210:213], v[174:177]
	v_mfma_f32_16x16x32_f16 v[178:181], v[242:245], v[214:217], v[178:181]
	v_mfma_f32_16x16x32_f16 v[154:157], v[242:245], v[218:221], v[154:157]
	s_setprio 0
	ds_read_b128 v[0:3], v130 offset:45056
	ds_read_b128 v[238:241], v130 offset:47104
	v_cvt_pk_f16_f32 v39, v38, v39
	v_cvt_pk_f16_f32 v38, v36, v37
	ds_write_b64 v100, v[38:39] offset:28672
	s_add_u32 s80, s22, 0xe0c00
	s_addc_u32 s81, s90, 0
	s_add_u32 s100, s22, 0xe0c00
	s_addc_u32 s101, s90, 0
	global_load_dwordx4 v[36:39], v201, s[100:101] nt
	s_setprio 1
	s_waitcnt lgkmcnt(1)
	v_mfma_f32_16x16x32_f16 v[20:23], v[0:3], v[206:209], v[20:23]
	v_mfma_f32_16x16x32_f16 v[234:237], v[0:3], v[210:213], v[234:237]
	v_mfma_f32_16x16x32_f16 v[158:161], v[0:3], v[214:217], v[158:161]
	v_mfma_f32_16x16x32_f16 v[166:169], v[0:3], v[218:221], v[166:169]
	v_mfma_f32_16x16x32_f16 v[182:185], v[238:241], v[206:209], v[182:185]
	v_mfma_f32_16x16x32_f16 v[190:193], v[238:241], v[210:213], v[190:193]
	v_mfma_f32_16x16x32_f16 v[202:205], v[238:241], v[214:217], v[202:205]
	v_mfma_f32_16x16x32_f16 v[186:189], v[238:241], v[218:221], v[186:189]
	s_setprio 0
	s_waitcnt vmcnt(6)
	s_waitcnt lgkmcnt(0)
	s_barrier
	ds_read_b128 v[206:209], v131
	ds_read_b128 v[210:213], v131 offset:2048
	ds_read_b128 v[214:217], v131 offset:4096
	ds_read_b128 v[218:221], v131 offset:6144
	ds_read_b128 v[238:241], v129
	ds_read_b128 v[242:245], v129 offset:2048
	s_add_u32 s80, s22, 0xd00
	v_lshl_add_u64 v[92:93], s[48:49], 0, v[196:197]
	s_addc_u32 s81, s90, 0
	s_mov_b32 m0, s0
	v_cvt_pk_f16_f32 v1, v6, v7
	global_load_lds_dwordx4 v[92:93], off
	v_cvt_pk_f16_f32 v0, v4, v5
	ds_write_b64 v100, v[0:1] offset:32768
	s_setprio 1
	s_waitcnt lgkmcnt(1)
	v_mfma_f32_16x16x32_f16 v[24:27], v[238:241], v[206:209], v[24:27]
	v_mfma_f32_16x16x32_f16 v[104:107], v[238:241], v[214:217], v[104:107]
	v_mfma_f32_16x16x32_f16 v[108:111], v[242:245], v[206:209], v[108:111]
	v_mfma_f32_16x16x32_f16 v[112:115], v[242:245], v[210:213], v[112:115]
	v_mfma_f32_16x16x32_f16 v[116:119], v[242:245], v[214:217], v[116:119]
	v_mfma_f32_16x16x32_f16 v[230:233], v[238:241], v[210:213], v[230:233]
	v_mfma_f32_16x16x32_f16 v[222:225], v[238:241], v[218:221], v[222:225]
	v_mfma_f32_16x16x32_f16 v[226:229], v[242:245], v[218:221], v[226:229]
	s_setprio 0
	ds_read_b128 v[238:241], v129 offset:4096
	ds_read_b128 v[242:245], v129 offset:6144
	s_mov_b32 m0, s72
	v_lshl_add_u64 v[4:5], v[92:93], 0, s[58:59]
	global_load_lds_dwordx4 v[4:5], off
	v_cvt_pk_f16_f32 v5, v66, v67
	v_cvt_pk_f16_f32 v4, v64, v65
	ds_write_b64 v100, v[4:5] offset:36864
	s_add_u32 s80, s22, 0x20d00
	s_addc_u32 s81, s90, 0
	s_add_u32 s100, s22, 0xd00
	s_addc_u32 s101, s90, 0
	global_load_dwordx4 v[0:3], v201, s[100:101] nt
	s_setprio 1
	s_waitcnt lgkmcnt(1)
	v_mfma_f32_16x16x32_f16 v[64:67], v[238:241], v[206:209], v[12:15]
	v_mfma_f32_16x16x32_f16 v[28:31], v[238:241], v[210:213], v[28:31]
	v_mfma_f32_16x16x32_f16 v[120:123], v[238:241], v[218:221], v[120:123]
	v_mfma_f32_16x16x32_f16 v[124:127], v[242:245], v[206:209], v[124:127]
	v_mfma_f32_16x16x32_f16 v[146:149], v[242:245], v[214:217], v[146:149]
	v_mfma_f32_16x16x32_f16 v[134:137], v[242:245], v[218:221], v[134:137]
	v_mfma_f32_16x16x32_f16 v[138:141], v[238:241], v[214:217], v[138:141]
	v_mfma_f32_16x16x32_f16 v[142:145], v[242:245], v[210:213], v[142:145]
	s_setprio 0
	ds_read_b128 v[238:241], v129 offset:8192
	ds_read_b128 v[242:245], v129 offset:10240
	s_mov_b32 m0, s71
	v_lshl_add_u64 v[12:13], v[92:93], 0, s[60:61]
	global_load_lds_dwordx4 v[12:13], off
	v_cvt_pk_f16_f32 v13, v42, v43
	v_cvt_pk_f16_f32 v12, v40, v41
	ds_write_b64 v100, v[12:13] offset:40960
	s_add_u32 s80, s22, 0x40d00
	s_addc_u32 s81, s90, 0
	s_add_u32 s100, s22, 0x20d00
	s_addc_u32 s101, s90, 0
	global_load_dwordx4 v[4:7], v201, s[100:101] nt
	s_setprio 1
	s_waitcnt lgkmcnt(1)
	v_mfma_f32_16x16x32_f16 v[40:43], v[238:241], v[206:209], v[16:19]
	v_mfma_f32_16x16x32_f16 v[32:35], v[238:241], v[210:213], v[32:35]
	v_mfma_f32_16x16x32_f16 v[170:173], v[238:241], v[214:217], v[170:173]
	v_mfma_f32_16x16x32_f16 v[150:153], v[238:241], v[218:221], v[150:153]
	v_mfma_f32_16x16x32_f16 v[162:165], v[242:245], v[206:209], v[162:165]
	v_mfma_f32_16x16x32_f16 v[174:177], v[242:245], v[210:213], v[174:177]
	v_mfma_f32_16x16x32_f16 v[178:181], v[242:245], v[214:217], v[178:181]
	v_mfma_f32_16x16x32_f16 v[154:157], v[242:245], v[218:221], v[154:157]
	s_setprio 0
	ds_read_b128 v[238:241], v129 offset:12288
	ds_read_b128 v[242:245], v129 offset:14336
	s_mov_b32 m0, s70
	v_lshl_add_u64 v[16:17], v[92:93], 0, s[62:63]
	global_load_lds_dwordx4 v[16:17], off
	v_cvt_pk_f16_f32 v17, v46, v47
	v_cvt_pk_f16_f32 v16, v44, v45
	ds_write_b64 v100, v[16:17] offset:45056
	s_add_u32 s70, s22, 0x60d00
	s_addc_u32 s71, s90, 0
	s_add_u32 s100, s22, 0x40d00
	s_addc_u32 s101, s90, 0
	global_load_dwordx4 v[12:15], v201, s[100:101] nt
	s_setprio 1
	s_waitcnt lgkmcnt(1)
	v_mfma_f32_16x16x32_f16 v[44:47], v[238:241], v[206:209], v[20:23]
	v_mfma_f32_16x16x32_f16 v[234:237], v[238:241], v[210:213], v[234:237]
	v_mfma_f32_16x16x32_f16 v[158:161], v[238:241], v[214:217], v[158:161]
	v_mfma_f32_16x16x32_f16 v[166:169], v[238:241], v[218:221], v[166:169]
	v_mfma_f32_16x16x32_f16 v[182:185], v[242:245], v[206:209], v[182:185]
	v_mfma_f32_16x16x32_f16 v[190:193], v[242:245], v[210:213], v[190:193]
	v_mfma_f32_16x16x32_f16 v[202:205], v[242:245], v[214:217], v[202:205]
	v_mfma_f32_16x16x32_f16 v[186:189], v[242:245], v[218:221], v[186:189]
	s_setprio 0
	ds_read_b128 v[206:209], v128
	ds_read_b128 v[210:213], v128 offset:2048
	ds_read_b128 v[214:217], v128 offset:4096
	ds_read_b128 v[218:221], v128 offset:6144
	ds_read_b128 v[238:241], v130
	ds_read_b128 v[242:245], v130 offset:2048
	v_cvt_pk_f16_f32 v21, v50, v51
	v_cvt_pk_f16_f32 v20, v48, v49
	ds_write_b64 v100, v[20:21] offset:49152
	s_add_u32 s70, s22, 0x80d00
	s_addc_u32 s71, s90, 0
	s_add_u32 s100, s22, 0x60d00
	s_addc_u32 s101, s90, 0
	global_load_dwordx4 v[16:19], v201, s[100:101] nt
	s_setprio 1
	s_waitcnt lgkmcnt(1)
	v_mfma_f32_16x16x32_f16 v[48:51], v[238:241], v[206:209], v[24:27]
	v_mfma_f32_16x16x32_f16 v[104:107], v[238:241], v[214:217], v[104:107]
	v_mfma_f32_16x16x32_f16 v[108:111], v[242:245], v[206:209], v[108:111]
	v_mfma_f32_16x16x32_f16 v[112:115], v[242:245], v[210:213], v[112:115]
	v_mfma_f32_16x16x32_f16 v[116:119], v[242:245], v[214:217], v[116:119]
	v_mfma_f32_16x16x32_f16 v[230:233], v[238:241], v[210:213], v[230:233]
	v_mfma_f32_16x16x32_f16 v[222:225], v[238:241], v[218:221], v[222:225]
	v_mfma_f32_16x16x32_f16 v[226:229], v[242:245], v[218:221], v[226:229]
	s_setprio 0
	ds_read_b128 v[238:241], v130 offset:4096
	ds_read_b128 v[242:245], v130 offset:6144
	v_cvt_pk_f16_f32 v25, v54, v55
	v_cvt_pk_f16_f32 v24, v52, v53
	ds_write_b64 v100, v[24:25] offset:53248
	s_add_u32 s70, s22, 0xa0d00
	s_addc_u32 s71, s90, 0
	s_add_u32 s100, s22, 0x80d00
	s_addc_u32 s101, s90, 0
	global_load_dwordx4 v[20:23], v201, s[100:101] nt
	s_setprio 1
	s_waitcnt lgkmcnt(1)
	v_mfma_f32_16x16x32_f16 v[52:55], v[238:241], v[206:209], v[64:67]
	v_mfma_f32_16x16x32_f16 v[64:67], v[238:241], v[210:213], v[28:31]
	v_mfma_f32_16x16x32_f16 v[120:123], v[238:241], v[218:221], v[120:123]
	v_mfma_f32_16x16x32_f16 v[124:127], v[242:245], v[206:209], v[124:127]
	v_mfma_f32_16x16x32_f16 v[146:149], v[242:245], v[214:217], v[146:149]
	v_mfma_f32_16x16x32_f16 v[134:137], v[242:245], v[218:221], v[134:137]
	v_mfma_f32_16x16x32_f16 v[138:141], v[238:241], v[214:217], v[138:141]
	v_mfma_f32_16x16x32_f16 v[142:145], v[242:245], v[210:213], v[142:145]
	s_setprio 0
	ds_read_b128 v[238:241], v130 offset:8192
	ds_read_b128 v[242:245], v130 offset:10240
	v_cvt_pk_f16_f32 v29, v58, v59
	v_cvt_pk_f16_f32 v28, v56, v57
	ds_write_b64 v100, v[28:29] offset:57344
	s_add_u32 s70, s22, 0xc0d00
	s_addc_u32 s71, s90, 0
	s_add_u32 s100, s22, 0xa0d00
	s_addc_u32 s101, s90, 0
	global_load_dwordx4 v[24:27], v201, s[100:101] nt
	s_add_u32 s100, s22, 0xc0d00
	s_addc_u32 s101, s90, 0
	global_load_dwordx4 v[28:31], v201, s[100:101] nt
	s_setprio 1
	s_waitcnt lgkmcnt(1)
	v_mfma_f32_16x16x32_f16 v[56:59], v[238:241], v[206:209], v[40:43]
	v_mfma_f32_16x16x32_f16 v[246:249], v[238:241], v[210:213], v[32:35]
	v_mfma_f32_16x16x32_f16 v[170:173], v[238:241], v[214:217], v[170:173]
	v_mfma_f32_16x16x32_f16 v[150:153], v[238:241], v[218:221], v[150:153]
	v_mfma_f32_16x16x32_f16 v[162:165], v[242:245], v[206:209], v[162:165]
	v_mfma_f32_16x16x32_f16 v[174:177], v[242:245], v[210:213], v[174:177]
	v_mfma_f32_16x16x32_f16 v[178:181], v[242:245], v[214:217], v[178:181]
	v_mfma_f32_16x16x32_f16 v[154:157], v[242:245], v[218:221], v[154:157]
	s_setprio 0
	ds_read_b128 v[40:43], v130 offset:12288
	ds_read_b128 v[238:241], v130 offset:14336
	v_cvt_pk_f16_f32 v33, v62, v63
	v_cvt_pk_f16_f32 v32, v60, v61
	ds_write_b64 v100, v[32:33] offset:61440
	s_add_u32 s70, s22, 0xe0d00
	s_addc_u32 s71, s90, 0
	s_add_u32 s100, s22, 0xe0d00
	s_addc_u32 s101, s90, 0
	global_load_dwordx4 v[32:35], v201, s[100:101] nt
	s_setprio 1
	s_waitcnt lgkmcnt(1)
	v_mfma_f32_16x16x32_f16 v[60:63], v[40:43], v[206:209], v[44:47]
	v_mfma_f32_16x16x32_f16 v[234:237], v[40:43], v[210:213], v[234:237]
	v_mfma_f32_16x16x32_f16 v[158:161], v[40:43], v[214:217], v[158:161]
	v_mfma_f32_16x16x32_f16 v[166:169], v[40:43], v[218:221], v[166:169]
	v_mfma_f32_16x16x32_f16 v[182:185], v[238:241], v[206:209], v[182:185]
	v_mfma_f32_16x16x32_f16 v[190:193], v[238:241], v[210:213], v[190:193]
	v_mfma_f32_16x16x32_f16 v[202:205], v[238:241], v[214:217], v[202:205]
	v_mfma_f32_16x16x32_f16 v[186:189], v[238:241], v[218:221], v[186:189]
	s_setprio 0
	s_waitcnt vmcnt(6)
	s_waitcnt lgkmcnt(0)
	s_barrier
	ds_read_b128 v[206:209], v131 offset:32768
	ds_read_b128 v[210:213], v131 offset:34816
	ds_read_b128 v[214:217], v131 offset:36864
	ds_read_b128 v[218:221], v131 offset:38912
	ds_read_b128 v[40:43], v129 offset:32768
	ds_read_b128 v[44:47], v129 offset:34816
	s_add_u32 s70, s22, 0xe00
	v_lshl_add_u64 v[92:93], s[50:51], 0, v[196:197]
	s_addc_u32 s71, s90, 0
	s_mov_b32 m0, s1
	v_cvt_pk_f16_f32 v11, v10, v11
	global_load_lds_dwordx4 v[92:93], off
	v_cvt_pk_f16_f32 v10, v8, v9
	ds_write_b64 v100, v[10:11]
	s_setprio 1
	s_waitcnt lgkmcnt(1)
	v_mfma_f32_16x16x32_f16 v[104:107], v[40:43], v[214:217], v[104:107]
	v_mfma_f32_16x16x32_f16 v[108:111], v[44:47], v[206:209], v[108:111]
	v_mfma_f32_16x16x32_f16 v[112:115], v[44:47], v[210:213], v[112:115]
	v_mfma_f32_16x16x32_f16 v[116:119], v[44:47], v[214:217], v[116:119]
	v_mfma_f32_16x16x32_f16 v[238:241], v[40:43], v[206:209], v[48:51]
	v_mfma_f32_16x16x32_f16 v[230:233], v[40:43], v[210:213], v[230:233]
	v_mfma_f32_16x16x32_f16 v[222:225], v[40:43], v[218:221], v[222:225]
	v_mfma_f32_16x16x32_f16 v[226:229], v[44:47], v[218:221], v[226:229]
	s_setprio 0
	ds_read_b128 v[44:47], v129 offset:36864
	ds_read_b128 v[48:51], v129 offset:38912
	s_mov_b32 m0, s92
	v_lshl_add_u64 v[40:41], v[92:93], 0, s[58:59]
	global_load_lds_dwordx4 v[40:41], off
	v_cvt_pk_f16_f32 v41, v70, v71
	v_cvt_pk_f16_f32 v40, v68, v69
	ds_write_b64 v100, v[40:41] offset:4096
	s_add_u32 s0, s22, 0x20e00
	s_addc_u32 s1, s90, 0
	s_add_u32 s100, s22, 0xe00
	s_addc_u32 s101, s90, 0
	global_load_dwordx4 v[8:11], v201, s[100:101] nt
	s_setprio 1
	s_waitcnt lgkmcnt(1)
	v_mfma_f32_16x16x32_f16 v[68:71], v[44:47], v[206:209], v[52:55]
	v_mfma_f32_16x16x32_f16 v[64:67], v[44:47], v[210:213], v[64:67]
	v_mfma_f32_16x16x32_f16 v[120:123], v[44:47], v[218:221], v[120:123]
	v_mfma_f32_16x16x32_f16 v[124:127], v[48:51], v[206:209], v[124:127]
	v_mfma_f32_16x16x32_f16 v[146:149], v[48:51], v[214:217], v[146:149]
	v_mfma_f32_16x16x32_f16 v[134:137], v[48:51], v[218:221], v[134:137]
	v_mfma_f32_16x16x32_f16 v[138:141], v[44:47], v[214:217], v[138:141]
	v_mfma_f32_16x16x32_f16 v[142:145], v[48:51], v[210:213], v[142:145]
	s_setprio 0
	ds_read_b128 v[48:51], v129 offset:40960
	ds_read_b128 v[52:55], v129 offset:43008
	s_mov_b32 m0, s91
	v_lshl_add_u64 v[44:45], v[92:93], 0, s[60:61]
	global_load_lds_dwordx4 v[44:45], off
	v_cvt_pk_f16_f32 v45, v74, v75
	v_cvt_pk_f16_f32 v44, v72, v73
	ds_write_b64 v100, v[44:45] offset:8192
	s_add_u32 s0, s22, 0x40e00
	s_addc_u32 s1, s90, 0
	s_add_u32 s100, s22, 0x20e00
	s_addc_u32 s101, s90, 0
	global_load_dwordx4 v[40:43], v201, s[100:101] nt
	s_setprio 1
	s_waitcnt lgkmcnt(1)
	v_mfma_f32_16x16x32_f16 v[72:75], v[48:51], v[206:209], v[56:59]
	v_mfma_f32_16x16x32_f16 v[242:245], v[48:51], v[210:213], v[246:249]
	v_mfma_f32_16x16x32_f16 v[170:173], v[48:51], v[214:217], v[170:173]
	v_mfma_f32_16x16x32_f16 v[150:153], v[48:51], v[218:221], v[150:153]
	v_mfma_f32_16x16x32_f16 v[162:165], v[52:55], v[206:209], v[162:165]
	v_mfma_f32_16x16x32_f16 v[174:177], v[52:55], v[210:213], v[174:177]
	v_mfma_f32_16x16x32_f16 v[178:181], v[52:55], v[214:217], v[178:181]
	v_mfma_f32_16x16x32_f16 v[154:157], v[52:55], v[218:221], v[154:157]
	s_setprio 0
	ds_read_b128 v[52:55], v129 offset:45056
	ds_read_b128 v[56:59], v129 offset:47104
	s_mov_b32 m0, s73
	v_lshl_add_u64 v[48:49], v[92:93], 0, s[62:63]
	global_load_lds_dwordx4 v[48:49], off
	v_cvt_pk_f16_f32 v49, v78, v79
	v_cvt_pk_f16_f32 v48, v76, v77
	ds_write_b64 v100, v[48:49] offset:12288
	s_add_u32 s0, s22, 0x60e00
	s_addc_u32 s1, s90, 0
	s_add_u32 s100, s22, 0x40e00
	s_addc_u32 s101, s90, 0
	global_load_dwordx4 v[44:47], v201, s[100:101] nt
	s_setprio 1
	s_waitcnt lgkmcnt(1)
	v_mfma_f32_16x16x32_f16 v[76:79], v[52:55], v[206:209], v[60:63]
	v_mfma_f32_16x16x32_f16 v[234:237], v[52:55], v[210:213], v[234:237]
	v_mfma_f32_16x16x32_f16 v[158:161], v[52:55], v[214:217], v[158:161]
	v_mfma_f32_16x16x32_f16 v[166:169], v[52:55], v[218:221], v[166:169]
	v_mfma_f32_16x16x32_f16 v[182:185], v[56:59], v[206:209], v[182:185]
	v_mfma_f32_16x16x32_f16 v[190:193], v[56:59], v[210:213], v[190:193]
	v_mfma_f32_16x16x32_f16 v[202:205], v[56:59], v[214:217], v[202:205]
	v_mfma_f32_16x16x32_f16 v[186:189], v[56:59], v[218:221], v[186:189]
	s_setprio 0
	ds_read_b128 v[206:209], v128 offset:32768
	ds_read_b128 v[210:213], v128 offset:34816
	ds_read_b128 v[214:217], v128 offset:36864
	ds_read_b128 v[218:221], v128 offset:38912
	ds_read_b128 v[56:59], v130 offset:32768
	ds_read_b128 v[60:63], v130 offset:34816
	v_cvt_pk_f16_f32 v53, v82, v83
	v_cvt_pk_f16_f32 v52, v80, v81
	ds_write_b64 v100, v[52:53] offset:16384
	s_add_u32 s0, s22, 0x80e00
	s_addc_u32 s1, s90, 0
	s_add_u32 s100, s22, 0x60e00
	s_addc_u32 s101, s90, 0
	global_load_dwordx4 v[48:51], v201, s[100:101] nt
	s_setprio 1
	s_waitcnt lgkmcnt(1)
	v_mfma_f32_16x16x32_f16 v[80:83], v[56:59], v[206:209], v[238:241]
	v_mfma_f32_16x16x32_f16 v[104:107], v[56:59], v[214:217], v[104:107]
	v_mfma_f32_16x16x32_f16 v[108:111], v[60:63], v[206:209], v[108:111]
	v_mfma_f32_16x16x32_f16 v[112:115], v[60:63], v[210:213], v[112:115]
	v_mfma_f32_16x16x32_f16 v[116:119], v[60:63], v[214:217], v[116:119]
	v_mfma_f32_16x16x32_f16 v[230:233], v[56:59], v[210:213], v[230:233]
	v_mfma_f32_16x16x32_f16 v[222:225], v[56:59], v[218:221], v[222:225]
	v_mfma_f32_16x16x32_f16 v[226:229], v[60:63], v[218:221], v[226:229]
	s_setprio 0
	ds_read_b128 v[60:63], v130 offset:36864
	ds_read_b128 v[238:241], v130 offset:38912
	v_cvt_pk_f16_f32 v57, v86, v87
	v_cvt_pk_f16_f32 v56, v84, v85
	ds_write_b64 v100, v[56:57] offset:20480
	s_add_u32 s0, s22, 0xa0e00
	s_addc_u32 s1, s90, 0
	s_add_u32 s100, s22, 0x80e00
	s_addc_u32 s101, s90, 0
	global_load_dwordx4 v[52:55], v201, s[100:101] nt
	s_setprio 1
	s_waitcnt lgkmcnt(1)
	v_mfma_f32_16x16x32_f16 v[68:71], v[60:63], v[206:209], v[68:71]
	v_mfma_f32_16x16x32_f16 v[64:67], v[60:63], v[210:213], v[64:67]
	v_mfma_f32_16x16x32_f16 v[84:87], v[60:63], v[214:217], v[138:141]
	v_mfma_f32_16x16x32_f16 v[120:123], v[60:63], v[218:221], v[120:123]
	v_mfma_f32_16x16x32_f16 v[124:127], v[238:241], v[206:209], v[124:127]
	v_mfma_f32_16x16x32_f16 v[134:137], v[238:241], v[218:221], v[134:137]
	v_mfma_f32_16x16x32_f16 v[138:141], v[238:241], v[210:213], v[142:145]
	v_mfma_f32_16x16x32_f16 v[142:145], v[238:241], v[214:217], v[146:149]
	s_setprio 0
	s_nop 1
	ds_read_b128 v[146:149], v130 offset:40960
	ds_read_b128 v[238:241], v130 offset:43008
	v_cvt_pk_f16_f32 v61, v90, v91
	v_cvt_pk_f16_f32 v60, v88, v89
	ds_write_b64 v100, v[60:61] offset:24576
	s_add_u32 s0, s22, 0xc0e00
	s_addc_u32 s1, s90, 0
	s_add_u32 s100, s22, 0xa0e00
	s_addc_u32 s101, s90, 0
	global_load_dwordx4 v[56:59], v201, s[100:101] nt
	s_add_u32 s100, s22, 0xc0e00
	s_addc_u32 s101, s90, 0
	global_load_dwordx4 v[60:63], v201, s[100:101] nt
	s_setprio 1
	s_waitcnt lgkmcnt(1)
	v_mfma_f32_16x16x32_f16 v[72:75], v[146:149], v[206:209], v[72:75]
	v_mfma_f32_16x16x32_f16 v[88:91], v[146:149], v[210:213], v[242:245]
	v_mfma_f32_16x16x32_f16 v[170:173], v[146:149], v[214:217], v[170:173]
	v_mfma_f32_16x16x32_f16 v[146:149], v[146:149], v[218:221], v[150:153]
	v_mfma_f32_16x16x32_f16 v[150:153], v[238:241], v[206:209], v[162:165]
	v_mfma_f32_16x16x32_f16 v[162:165], v[238:241], v[210:213], v[174:177]
	v_mfma_f32_16x16x32_f16 v[174:177], v[238:241], v[214:217], v[178:181]
	v_mfma_f32_16x16x32_f16 v[154:157], v[238:241], v[218:221], v[154:157]
	s_setprio 0
	s_nop 0
	ds_read_b128 v[178:181], v130 offset:45056
	ds_read_b128 v[238:241], v130 offset:47104
	v_cvt_pk_f16_f32 v39, v38, v39
	v_cvt_pk_f16_f32 v38, v36, v37
	ds_write_b64 v100, v[38:39] offset:28672
	s_add_u32 s0, s22, 0xe0e00
	s_addc_u32 s1, s90, 0
	s_add_u32 s100, s22, 0xe0e00
	s_addc_u32 s101, s90, 0
	global_load_dwordx4 v[36:39], v201, s[100:101] nt
	s_setprio 1
	s_waitcnt lgkmcnt(1)
	v_mfma_f32_16x16x32_f16 v[76:79], v[178:181], v[206:209], v[76:79]
	v_mfma_f32_16x16x32_f16 v[234:237], v[178:181], v[210:213], v[234:237]
	v_mfma_f32_16x16x32_f16 v[158:161], v[178:181], v[214:217], v[158:161]
	v_mfma_f32_16x16x32_f16 v[166:169], v[178:181], v[218:221], v[166:169]
	v_mfma_f32_16x16x32_f16 v[178:181], v[238:241], v[206:209], v[182:185]
	v_mfma_f32_16x16x32_f16 v[182:185], v[238:241], v[210:213], v[190:193]
	v_mfma_f32_16x16x32_f16 v[190:193], v[238:241], v[214:217], v[202:205]
	v_mfma_f32_16x16x32_f16 v[186:189], v[238:241], v[218:221], v[186:189]
	s_setprio 0
	s_waitcnt vmcnt(6)
	s_waitcnt lgkmcnt(0)
	s_barrier
	ds_read_b128 v[202:205], v131
	ds_read_b128 v[206:209], v131 offset:2048
	ds_read_b128 v[210:213], v131 offset:4096
	ds_read_b128 v[214:217], v131 offset:6144
	ds_read_b128 v[218:221], v129
	ds_read_b128 v[238:241], v129 offset:2048
	s_add_u32 s70, s22, 0xf00
	v_lshl_add_u64 v[92:93], s[52:53], 0, v[196:197]
	s_addc_u32 s71, s90, 0
	v_readfirstlane_b32 s0, v95
	s_mov_b32 m0, s0
	v_cvt_pk_f16_f32 v3, v2, v3
	global_load_lds_dwordx4 v[92:93], off
	v_cvt_pk_f16_f32 v2, v0, v1
	ds_write_b64 v100, v[2:3] offset:32768
	s_setprio 1
	s_waitcnt lgkmcnt(1)
	v_mfma_f32_16x16x32_f16 v[80:83], v[218:221], v[202:205], v[80:83]
	v_mfma_f32_16x16x32_f16 v[104:107], v[218:221], v[210:213], v[104:107]
	v_mfma_f32_16x16x32_f16 v[108:111], v[238:241], v[202:205], v[108:111]
	v_mfma_f32_16x16x32_f16 v[112:115], v[238:241], v[206:209], v[112:115]
	v_mfma_f32_16x16x32_f16 v[116:119], v[238:241], v[210:213], v[116:119]
	v_mfma_f32_16x16x32_f16 v[230:233], v[218:221], v[206:209], v[230:233]
	v_mfma_f32_16x16x32_f16 v[218:221], v[218:221], v[214:217], v[222:225]
	v_mfma_f32_16x16x32_f16 v[222:225], v[238:241], v[214:217], v[226:229]
	s_setprio 0
	s_nop 1
	ds_read_b128 v[226:229], v129 offset:4096
	ds_read_b128 v[238:241], v129 offset:6144
	v_readfirstlane_b32 s1, v96
	v_lshl_add_u64 v[198:199], v[92:93], 0, s[58:59]
	s_mov_b32 m0, s1
	v_cvt_pk_f16_f32 v7, v6, v7
	global_load_lds_dwordx4 v[198:199], off
	v_cvt_pk_f16_f32 v6, v4, v5
	ds_write_b64 v100, v[6:7] offset:36864
	s_add_u32 s70, s22, 0x20f00
	s_addc_u32 s71, s90, 0
	s_add_u32 s100, s22, 0xf00
	s_addc_u32 s101, s90, 0
	global_load_dwordx4 v[0:3], v201, s[100:101] nt
	s_setprio 1
	s_waitcnt lgkmcnt(1)
	v_mfma_f32_16x16x32_f16 v[68:71], v[226:229], v[202:205], v[68:71]
	v_mfma_f32_16x16x32_f16 v[64:67], v[226:229], v[206:209], v[64:67]
	v_mfma_f32_16x16x32_f16 v[84:87], v[226:229], v[210:213], v[84:87]
	v_mfma_f32_16x16x32_f16 v[120:123], v[226:229], v[214:217], v[120:123]
	v_mfma_f32_16x16x32_f16 v[124:127], v[238:241], v[202:205], v[124:127]
	v_mfma_f32_16x16x32_f16 v[134:137], v[238:241], v[214:217], v[134:137]
	v_mfma_f32_16x16x32_f16 v[138:141], v[238:241], v[206:209], v[138:141]
	v_mfma_f32_16x16x32_f16 v[142:145], v[238:241], v[210:213], v[142:145]
	s_setprio 0
	ds_read_b128 v[226:229], v129 offset:8192
	ds_read_b128 v[238:241], v129 offset:10240
	v_readfirstlane_b32 s70, v97
	v_lshl_add_u64 v[198:199], v[92:93], 0, s[60:61]
	s_mov_b32 m0, s70
	v_cvt_pk_f16_f32 v15, v14, v15
	global_load_lds_dwordx4 v[198:199], off
	v_cvt_pk_f16_f32 v14, v12, v13
	ds_write_b64 v100, v[14:15] offset:40960
	s_add_u32 s72, s22, 0x40f00
	s_addc_u32 s73, s90, 0
	s_add_u32 s100, s22, 0x20f00
	s_addc_u32 s101, s90, 0
	global_load_dwordx4 v[4:7], v201, s[100:101] nt
	s_setprio 1
	s_waitcnt lgkmcnt(1)
	v_mfma_f32_16x16x32_f16 v[72:75], v[226:229], v[202:205], v[72:75]
	v_mfma_f32_16x16x32_f16 v[88:91], v[226:229], v[206:209], v[88:91]
	v_mfma_f32_16x16x32_f16 v[146:149], v[226:229], v[214:217], v[146:149]
	v_mfma_f32_16x16x32_f16 v[170:173], v[226:229], v[210:213], v[170:173]
	v_mfma_f32_16x16x32_f16 v[150:153], v[238:241], v[202:205], v[150:153]
	v_mfma_f32_16x16x32_f16 v[162:165], v[238:241], v[206:209], v[162:165]
	v_mfma_f32_16x16x32_f16 v[174:177], v[238:241], v[210:213], v[174:177]
	v_mfma_f32_16x16x32_f16 v[154:157], v[238:241], v[214:217], v[154:157]
	s_setprio 0
	ds_read_b128 v[226:229], v129 offset:12288
	ds_read_b128 v[238:241], v129 offset:14336
	v_readfirstlane_b32 s71, v98
	v_lshl_add_u64 v[92:93], v[92:93], 0, s[62:63]
	s_mov_b32 m0, s71
	v_cvt_pk_f16_f32 v19, v18, v19
	global_load_lds_dwordx4 v[92:93], off
	v_cvt_pk_f16_f32 v18, v16, v17
	ds_write_b64 v100, v[18:19] offset:45056
	s_add_u32 s72, s22, 0x60f00
	s_addc_u32 s73, s90, 0
	s_add_u32 s100, s22, 0x40f00
	s_addc_u32 s101, s90, 0
	global_load_dwordx4 v[12:15], v201, s[100:101] nt
	s_setprio 1
	s_waitcnt lgkmcnt(1)
	v_mfma_f32_16x16x32_f16 v[76:79], v[226:229], v[202:205], v[76:79]
	v_mfma_f32_16x16x32_f16 v[234:237], v[226:229], v[206:209], v[234:237]
	v_mfma_f32_16x16x32_f16 v[158:161], v[226:229], v[210:213], v[158:161]
	v_mfma_f32_16x16x32_f16 v[166:169], v[226:229], v[214:217], v[166:169]
	v_mfma_f32_16x16x32_f16 v[178:181], v[238:241], v[202:205], v[178:181]
	v_mfma_f32_16x16x32_f16 v[182:185], v[238:241], v[206:209], v[182:185]
	v_mfma_f32_16x16x32_f16 v[190:193], v[238:241], v[210:213], v[190:193]
	v_mfma_f32_16x16x32_f16 v[186:189], v[238:241], v[214:217], v[186:189]
	s_setprio 0
	ds_read_b128 v[202:205], v128
	ds_read_b128 v[206:209], v128 offset:2048
	ds_read_b128 v[210:213], v128 offset:4096
	ds_read_b128 v[214:217], v128 offset:6144
	ds_read_b128 v[226:229], v130
	ds_read_b128 v[238:241], v130 offset:2048
	v_cvt_pk_f16_f32 v23, v22, v23
	v_cvt_pk_f16_f32 v22, v20, v21
	ds_write_b64 v100, v[22:23] offset:49152
	s_add_u32 s72, s22, 0x80f00
	s_addc_u32 s73, s90, 0
	s_add_u32 s100, s22, 0x60f00
	s_addc_u32 s101, s90, 0
	global_load_dwordx4 v[16:19], v201, s[100:101] nt
	s_setprio 1
	s_waitcnt lgkmcnt(1)
	v_mfma_f32_16x16x32_f16 v[80:83], v[226:229], v[202:205], v[80:83]
	v_mfma_f32_16x16x32_f16 v[104:107], v[226:229], v[210:213], v[104:107]
	v_mfma_f32_16x16x32_f16 v[108:111], v[238:241], v[202:205], v[108:111]
	v_mfma_f32_16x16x32_f16 v[112:115], v[238:241], v[206:209], v[112:115]
	v_mfma_f32_16x16x32_f16 v[116:119], v[238:241], v[210:213], v[116:119]
	v_mfma_f32_16x16x32_f16 v[230:233], v[226:229], v[206:209], v[230:233]
	v_mfma_f32_16x16x32_f16 v[218:221], v[226:229], v[214:217], v[218:221]
	v_mfma_f32_16x16x32_f16 v[222:225], v[238:241], v[214:217], v[222:225]
	s_setprio 0
	ds_read_b128 v[226:229], v130 offset:4096
	ds_read_b128 v[238:241], v130 offset:6144
	v_cvt_pk_f16_f32 v27, v26, v27
	v_cvt_pk_f16_f32 v26, v24, v25
	ds_write_b64 v100, v[26:27] offset:53248
	s_add_u32 s72, s22, 0xa0f00
	s_addc_u32 s73, s90, 0
	s_add_u32 s100, s22, 0x80f00
	s_addc_u32 s101, s90, 0
	global_load_dwordx4 v[20:23], v201, s[100:101] nt
	s_setprio 1
	s_waitcnt lgkmcnt(1)
	v_mfma_f32_16x16x32_f16 v[68:71], v[226:229], v[202:205], v[68:71]
	v_mfma_f32_16x16x32_f16 v[64:67], v[226:229], v[206:209], v[64:67]
	v_mfma_f32_16x16x32_f16 v[84:87], v[226:229], v[210:213], v[84:87]
	v_mfma_f32_16x16x32_f16 v[120:123], v[226:229], v[214:217], v[120:123]
	v_mfma_f32_16x16x32_f16 v[124:127], v[238:241], v[202:205], v[124:127]
	v_mfma_f32_16x16x32_f16 v[134:137], v[238:241], v[214:217], v[134:137]
	v_mfma_f32_16x16x32_f16 v[138:141], v[238:241], v[206:209], v[138:141]
	v_mfma_f32_16x16x32_f16 v[142:145], v[238:241], v[210:213], v[142:145]
	s_setprio 0
	ds_read_b128 v[226:229], v130 offset:8192
	ds_read_b128 v[238:241], v130 offset:10240
	v_cvt_pk_f16_f32 v31, v30, v31
	v_cvt_pk_f16_f32 v30, v28, v29
	ds_write_b64 v100, v[30:31] offset:57344
	s_add_u32 s72, s22, 0xc0f00
	s_addc_u32 s73, s90, 0
	s_add_u32 s100, s22, 0xa0f00
	s_addc_u32 s101, s90, 0
	global_load_dwordx4 v[24:27], v201, s[100:101] nt
	s_add_u32 s100, s22, 0xc0f00
	s_addc_u32 s101, s90, 0
	global_load_dwordx4 v[28:31], v201, s[100:101] nt
	s_setprio 1
	s_waitcnt lgkmcnt(1)
	v_mfma_f32_16x16x32_f16 v[72:75], v[226:229], v[202:205], v[72:75]
	v_mfma_f32_16x16x32_f16 v[88:91], v[226:229], v[206:209], v[88:91]
	v_mfma_f32_16x16x32_f16 v[146:149], v[226:229], v[214:217], v[146:149]
	v_mfma_f32_16x16x32_f16 v[170:173], v[226:229], v[210:213], v[170:173]
	v_mfma_f32_16x16x32_f16 v[150:153], v[238:241], v[202:205], v[150:153]
	v_mfma_f32_16x16x32_f16 v[162:165], v[238:241], v[206:209], v[162:165]
	v_mfma_f32_16x16x32_f16 v[174:177], v[238:241], v[210:213], v[174:177]
	v_mfma_f32_16x16x32_f16 v[154:157], v[238:241], v[214:217], v[154:157]
	s_setprio 0
	ds_read_b128 v[226:229], v130 offset:12288
	ds_read_b128 v[238:241], v130 offset:14336
	v_cvt_pk_f16_f32 v35, v34, v35
	v_cvt_pk_f16_f32 v34, v32, v33
	ds_write_b64 v100, v[34:35] offset:61440
	s_add_u32 s72, s22, 0xe0f00
	s_addc_u32 s73, s90, 0
	s_add_u32 s100, s22, 0xe0f00
	s_addc_u32 s101, s90, 0
	global_load_dwordx4 v[32:35], v201, s[100:101] nt
	s_setprio 1
	s_waitcnt lgkmcnt(1)
	v_mfma_f32_16x16x32_f16 v[76:79], v[226:229], v[202:205], v[76:79]
	v_mfma_f32_16x16x32_f16 v[234:237], v[226:229], v[206:209], v[234:237]
	v_mfma_f32_16x16x32_f16 v[158:161], v[226:229], v[210:213], v[158:161]
	v_mfma_f32_16x16x32_f16 v[166:169], v[226:229], v[214:217], v[166:169]
	v_mfma_f32_16x16x32_f16 v[178:181], v[238:241], v[202:205], v[178:181]
	v_mfma_f32_16x16x32_f16 v[182:185], v[238:241], v[206:209], v[182:185]
	v_mfma_f32_16x16x32_f16 v[190:193], v[238:241], v[210:213], v[190:193]
	v_mfma_f32_16x16x32_f16 v[186:189], v[238:241], v[214:217], v[186:189]
	s_setprio 0
	s_waitcnt vmcnt(6)
	s_waitcnt lgkmcnt(0)
	s_barrier
	ds_read_b128 v[202:205], v131 offset:32768
	ds_read_b128 v[206:209], v131 offset:34816
	ds_read_b128 v[210:213], v131 offset:36864
	ds_read_b128 v[214:217], v131 offset:38912
	ds_read_b128 v[226:229], v129 offset:32768
	ds_read_b128 v[238:241], v129 offset:34816
	v_lshl_add_u64 v[198:199], s[54:55], 0, v[196:197]
	v_readfirstlane_b32 s64, v94
	s_mov_b32 m0, s64
	v_cvt_pk_f16_f32 v11, v10, v11
	global_load_lds_dwordx4 v[198:199], off
	v_cvt_pk_f16_f32 v10, v8, v9
	ds_write_b64 v100, v[10:11]
	s_setprio 1
	s_waitcnt lgkmcnt(1)
	v_mfma_f32_16x16x32_f16 v[8:11], v[226:229], v[202:205], v[80:83]
	v_mfma_f32_16x16x32_f16 v[80:83], v[226:229], v[206:209], v[230:233]
	v_mfma_f32_16x16x32_f16 v[92:95], v[226:229], v[210:213], v[104:107]
	v_mfma_f32_16x16x32_f16 v[104:107], v[226:229], v[214:217], v[218:221]
	v_mfma_f32_16x16x32_f16 v[108:111], v[238:241], v[202:205], v[108:111]
	v_mfma_f32_16x16x32_f16 v[112:115], v[238:241], v[206:209], v[112:115]
	v_mfma_f32_16x16x32_f16 v[116:119], v[238:241], v[210:213], v[116:119]
	v_mfma_f32_16x16x32_f16 v[218:221], v[238:241], v[214:217], v[222:225]
	s_setprio 0
	s_nop 1
	ds_read_b128 v[222:225], v129 offset:36864
	ds_read_b128 v[226:229], v129 offset:38912
	v_readfirstlane_b32 s64, v99
	v_lshl_add_u64 v[96:97], v[198:199], 0, s[58:59]
	s_mov_b32 m0, s64
	v_cvt_pk_f16_f32 v43, v42, v43
	global_load_lds_dwordx4 v[96:97], off
	v_cvt_pk_f16_f32 v42, v40, v41
	ds_write_b64 v100, v[42:43] offset:4096
	s_setprio 1
	s_waitcnt lgkmcnt(1)
	v_mfma_f32_16x16x32_f16 v[40:43], v[222:225], v[202:205], v[68:71]
	v_mfma_f32_16x16x32_f16 v[64:67], v[222:225], v[206:209], v[64:67]
	v_mfma_f32_16x16x32_f16 v[68:71], v[222:225], v[210:213], v[84:87]
	v_mfma_f32_16x16x32_f16 v[84:87], v[222:225], v[214:217], v[120:123]
	v_mfma_f32_16x16x32_f16 v[96:99], v[226:229], v[202:205], v[124:127]
	v_mfma_f32_16x16x32_f16 v[120:123], v[226:229], v[206:209], v[138:141]
	v_mfma_f32_16x16x32_f16 v[124:127], v[226:229], v[210:213], v[142:145]
	v_mfma_f32_16x16x32_f16 v[134:137], v[226:229], v[214:217], v[134:137]
	s_setprio 0
	ds_read_b128 v[138:141], v129 offset:40960
	ds_read_b128 v[142:145], v129 offset:43008
	v_readfirstlane_b32 s64, v101
	v_lshl_add_u64 v[222:223], v[198:199], 0, s[60:61]
	s_mov_b32 m0, s64
	v_cvt_pk_f16_f32 v47, v46, v47
	global_load_lds_dwordx4 v[222:223], off
	v_cvt_pk_f16_f32 v46, v44, v45
	ds_write_b64 v100, v[46:47] offset:8192
	s_setprio 1
	s_waitcnt lgkmcnt(1)
	v_mfma_f32_16x16x32_f16 v[44:47], v[138:141], v[202:205], v[72:75]
	v_mfma_f32_16x16x32_f16 v[72:75], v[138:141], v[206:209], v[88:91]
	v_mfma_f32_16x16x32_f16 v[88:91], v[138:141], v[210:213], v[170:173]
	v_mfma_f32_16x16x32_f16 v[138:141], v[138:141], v[214:217], v[146:149]
	v_mfma_f32_16x16x32_f16 v[146:149], v[142:145], v[202:205], v[150:153]
	v_mfma_f32_16x16x32_f16 v[150:153], v[142:145], v[206:209], v[162:165]
	v_mfma_f32_16x16x32_f16 v[162:165], v[142:145], v[210:213], v[174:177]
	v_mfma_f32_16x16x32_f16 v[142:145], v[142:145], v[214:217], v[154:157]
	s_setprio 0
	s_nop 1
	ds_read_b128 v[154:157], v129 offset:45056
	ds_read_b128 v[170:173], v129 offset:47104
	v_readfirstlane_b32 s64, v102
	v_lshl_add_u64 v[174:175], v[198:199], 0, s[62:63]
	s_mov_b32 m0, s64
	v_cvt_pk_f16_f32 v51, v50, v51
	global_load_lds_dwordx4 v[174:175], off
	v_cvt_pk_f16_f32 v50, v48, v49
	ds_write_b64 v100, v[50:51] offset:12288
	s_setprio 1
	s_waitcnt lgkmcnt(1)
	v_mfma_f32_16x16x32_f16 v[48:51], v[154:157], v[202:205], v[76:79]
	v_mfma_f32_16x16x32_f16 v[76:79], v[154:157], v[206:209], v[234:237]
	v_mfma_f32_16x16x32_f16 v[158:161], v[154:157], v[210:213], v[158:161]
	v_mfma_f32_16x16x32_f16 v[154:157], v[154:157], v[214:217], v[166:169]
	v_mfma_f32_16x16x32_f16 v[166:169], v[170:173], v[202:205], v[178:181]
	v_mfma_f32_16x16x32_f16 v[174:177], v[170:173], v[206:209], v[182:185]
	v_mfma_f32_16x16x32_f16 v[178:181], v[170:173], v[210:213], v[190:193]
	v_mfma_f32_16x16x32_f16 v[170:173], v[170:173], v[214:217], v[186:189]
	s_setprio 0
	ds_read_b128 v[182:185], v128 offset:32768
	s_nop 0
	ds_read_b128 v[186:189], v128 offset:34816
	ds_read_b128 v[190:193], v128 offset:36864
	ds_read_b128 v[202:205], v128 offset:38912
	ds_read_b128 v[206:209], v130 offset:32768
	ds_read_b128 v[210:213], v130 offset:34816
	v_cvt_pk_f16_f32 v55, v54, v55
	v_cvt_pk_f16_f32 v54, v52, v53
	ds_write_b64 v100, v[54:55] offset:16384
	s_setprio 1
	s_waitcnt lgkmcnt(1)
	v_mfma_f32_16x16x32_f16 v[8:11], v[206:209], v[182:185], v[8:11]
	v_mfma_f32_16x16x32_f16 v[52:55], v[206:209], v[186:189], v[80:83]
	v_mfma_f32_16x16x32_f16 v[80:83], v[206:209], v[190:193], v[92:95]
	v_mfma_f32_16x16x32_f16 v[92:95], v[206:209], v[202:205], v[104:107]
	v_mfma_f32_16x16x32_f16 v[102:105], v[210:213], v[182:185], v[108:111]
	v_mfma_f32_16x16x32_f16 v[106:109], v[210:213], v[186:189], v[112:115]
	v_mfma_f32_16x16x32_f16 v[110:113], v[210:213], v[190:193], v[116:119]
	v_mfma_f32_16x16x32_f16 v[114:117], v[210:213], v[202:205], v[218:221]
	s_setprio 0
	ds_read_b128 v[206:209], v130 offset:36864
	ds_read_b128 v[210:213], v130 offset:38912
	v_cvt_pk_f16_f32 v59, v58, v59
	v_cvt_pk_f16_f32 v58, v56, v57
	ds_write_b64 v100, v[58:59] offset:20480
	s_setprio 1
	s_waitcnt lgkmcnt(1)
	v_mfma_f32_16x16x32_f16 v[40:43], v[206:209], v[182:185], v[40:43]
	v_mfma_f32_16x16x32_f16 v[56:59], v[206:209], v[186:189], v[64:67]
	v_mfma_f32_16x16x32_f16 v[64:67], v[206:209], v[190:193], v[68:71]
	v_mfma_f32_16x16x32_f16 v[68:71], v[206:209], v[202:205], v[84:87]
	v_mfma_f32_16x16x32_f16 v[84:87], v[210:213], v[182:185], v[96:99]
	v_mfma_f32_16x16x32_f16 v[96:99], v[210:213], v[186:189], v[120:123]
	v_mfma_f32_16x16x32_f16 v[118:121], v[210:213], v[190:193], v[124:127]
	v_mfma_f32_16x16x32_f16 v[122:125], v[210:213], v[202:205], v[134:137]
	s_setprio 0
	s_nop 1
	ds_read_b128 v[134:137], v130 offset:40960
	ds_read_b128 v[206:209], v130 offset:43008
	v_cvt_pk_f16_f32 v63, v62, v63
	v_cvt_pk_f16_f32 v62, v60, v61
	ds_write_b64 v100, v[62:63] offset:24576
	s_setprio 1
	s_waitcnt lgkmcnt(1)
	v_mfma_f32_16x16x32_f16 v[44:47], v[134:137], v[182:185], v[44:47]
	v_mfma_f32_16x16x32_f16 v[60:63], v[134:137], v[186:189], v[72:75]
	v_mfma_f32_16x16x32_f16 v[72:75], v[134:137], v[190:193], v[88:91]
	v_mfma_f32_16x16x32_f16 v[88:91], v[134:137], v[202:205], v[138:141]
	v_mfma_f32_16x16x32_f16 v[134:137], v[206:209], v[182:185], v[146:149]
	v_mfma_f32_16x16x32_f16 v[146:149], v[206:209], v[190:193], v[162:165]
	v_mfma_f32_16x16x32_f16 v[138:141], v[206:209], v[186:189], v[150:153]
	v_mfma_f32_16x16x32_f16 v[142:145], v[206:209], v[202:205], v[142:145]
	s_setprio 0
	s_nop 0
	ds_read_b128 v[150:153], v130 offset:45056
	ds_read_b128 v[162:165], v130 offset:47104
	v_cvt_pk_f16_f32 v39, v38, v39
	v_cvt_pk_f16_f32 v38, v36, v37
	ds_write_b64 v100, v[38:39] offset:28672
	s_setprio 1
	s_waitcnt lgkmcnt(1)
	v_mfma_f32_16x16x32_f16 v[36:39], v[150:153], v[182:185], v[48:51]
	v_mfma_f32_16x16x32_f16 v[48:51], v[150:153], v[186:189], v[76:79]
	v_mfma_f32_16x16x32_f16 v[76:79], v[150:153], v[190:193], v[158:161]
	v_mfma_f32_16x16x32_f16 v[150:153], v[150:153], v[202:205], v[154:157]
	v_mfma_f32_16x16x32_f16 v[154:157], v[162:165], v[182:185], v[166:169]
	v_mfma_f32_16x16x32_f16 v[158:161], v[162:165], v[186:189], v[174:177]
	v_mfma_f32_16x16x32_f16 v[166:169], v[162:165], v[190:193], v[178:181]
	v_mfma_f32_16x16x32_f16 v[162:165], v[162:165], v[202:205], v[170:173]
	s_setprio 0
	s_waitcnt vmcnt(0)
	s_waitcnt lgkmcnt(0)
	s_barrier
	s_nop 0
	ds_read_b128 v[170:173], v131
	ds_read_b128 v[174:177], v131 offset:2048
	ds_read_b128 v[178:181], v131 offset:4096
	ds_read_b128 v[182:185], v131 offset:6144
	ds_read_b128 v[186:189], v129
	ds_read_b128 v[190:193], v129 offset:2048
	v_lshl_add_u64 v[126:127], s[56:57], 0, v[196:197]
	s_mov_b32 m0, s0
	v_cvt_pk_f16_f32 v3, v2, v3
	global_load_lds_dwordx4 v[126:127], off
	v_cvt_pk_f16_f32 v2, v0, v1
	ds_write_b64 v100, v[2:3] offset:32768
	s_setprio 1
	s_waitcnt lgkmcnt(1)
	v_mfma_f32_16x16x32_f16 v[0:3], v[186:189], v[170:173], v[8:11]
	v_mfma_f32_16x16x32_f16 v[8:11], v[186:189], v[174:177], v[52:55]
	v_mfma_f32_16x16x32_f16 v[52:55], v[186:189], v[178:181], v[80:83]
	v_mfma_f32_16x16x32_f16 v[80:83], v[186:189], v[182:185], v[92:95]
	v_mfma_f32_16x16x32_f16 v[92:95], v[190:193], v[170:173], v[102:105]
	v_mfma_f32_16x16x32_f16 v[102:105], v[190:193], v[174:177], v[106:109]
	v_mfma_f32_16x16x32_f16 v[106:109], v[190:193], v[178:181], v[110:113]
	v_mfma_f32_16x16x32_f16 v[110:113], v[190:193], v[182:185], v[114:117]
	s_setprio 0
	s_nop 1
	ds_read_b128 v[114:117], v129 offset:4096
	ds_read_b128 v[186:189], v129 offset:6144
	s_mov_b32 m0, s1
	v_lshl_add_u64 v[190:191], v[126:127], 0, s[58:59]
	global_load_lds_dwordx4 v[190:191], off
	v_cvt_pk_f16_f32 v7, v6, v7
	v_cvt_pk_f16_f32 v6, v4, v5
	ds_write_b64 v100, v[6:7] offset:36864
	s_setprio 1
	s_waitcnt lgkmcnt(1)
	v_mfma_f32_16x16x32_f16 v[190:193], v[114:117], v[170:173], v[40:43]
	v_mfma_f32_16x16x32_f16 v[56:59], v[114:117], v[174:177], v[56:59]
	v_mfma_f32_16x16x32_f16 v[64:67], v[114:117], v[178:181], v[64:67]
	v_mfma_f32_16x16x32_f16 v[68:71], v[114:117], v[182:185], v[68:71]
	v_mfma_f32_16x16x32_f16 v[84:87], v[186:189], v[170:173], v[84:87]
	v_mfma_f32_16x16x32_f16 v[96:99], v[186:189], v[174:177], v[96:99]
	v_mfma_f32_16x16x32_f16 v[114:117], v[186:189], v[178:181], v[118:121]
	v_mfma_f32_16x16x32_f16 v[118:121], v[186:189], v[182:185], v[122:125]
	s_setprio 0
	ds_read_b128 v[4:7], v129 offset:8192
	ds_read_b128 v[40:43], v129 offset:10240
	s_mov_b32 m0, s70
	v_lshl_add_u64 v[122:123], v[126:127], 0, s[60:61]
	global_load_lds_dwordx4 v[122:123], off
	v_cvt_pk_f16_f32 v15, v14, v15
	v_cvt_pk_f16_f32 v14, v12, v13
	ds_write_b64 v100, v[14:15] offset:40960
	s_setprio 1
	s_waitcnt lgkmcnt(1)
	v_mfma_f32_16x16x32_f16 v[122:125], v[4:7], v[170:173], v[44:47]
	v_mfma_f32_16x16x32_f16 v[88:91], v[4:7], v[182:185], v[88:91]
	v_mfma_f32_16x16x32_f16 v[134:137], v[40:43], v[170:173], v[134:137]
	v_mfma_f32_16x16x32_f16 v[146:149], v[40:43], v[178:181], v[146:149]
	v_mfma_f32_16x16x32_f16 v[186:189], v[4:7], v[174:177], v[60:63]
	v_mfma_f32_16x16x32_f16 v[202:205], v[4:7], v[178:181], v[72:75]
	v_mfma_f32_16x16x32_f16 v[138:141], v[40:43], v[174:177], v[138:141]
	v_mfma_f32_16x16x32_f16 v[142:145], v[40:43], v[182:185], v[142:145]
	s_setprio 0
	ds_read_b128 v[4:7], v129 offset:12288
	ds_read_b128 v[12:15], v129 offset:14336
	s_mov_b32 m0, s71
	v_lshl_add_u64 v[40:41], v[126:127], 0, s[62:63]
	global_load_lds_dwordx4 v[40:41], off
	v_cvt_pk_f16_f32 v19, v18, v19
	v_cvt_pk_f16_f32 v18, v16, v17
	ds_write_b64 v100, v[18:19] offset:45056
	s_setprio 1
	s_waitcnt lgkmcnt(1)
	v_mfma_f32_16x16x32_f16 v[206:209], v[4:7], v[170:173], v[36:39]
	v_mfma_f32_16x16x32_f16 v[210:213], v[4:7], v[174:177], v[48:51]
	v_mfma_f32_16x16x32_f16 v[214:217], v[4:7], v[178:181], v[76:79]
	v_mfma_f32_16x16x32_f16 v[150:153], v[4:7], v[182:185], v[150:153]
	v_mfma_f32_16x16x32_f16 v[154:157], v[12:15], v[170:173], v[154:157]
	v_mfma_f32_16x16x32_f16 v[158:161], v[12:15], v[174:177], v[158:161]
	v_mfma_f32_16x16x32_f16 v[166:169], v[12:15], v[178:181], v[166:169]
	v_mfma_f32_16x16x32_f16 v[162:165], v[12:15], v[182:185], v[162:165]
	s_setprio 0
	ds_read_b128 v[170:173], v128
	ds_read_b128 v[174:177], v128 offset:2048
	ds_read_b128 v[178:181], v128 offset:4096
	ds_read_b128 v[182:185], v128 offset:6144
	ds_read_b128 v[12:15], v130
	ds_read_b128 v[40:43], v130 offset:2048
	v_cvt_pk_f16_f32 v5, v22, v23
	v_cvt_pk_f16_f32 v4, v20, v21
	ds_write_b64 v100, v[4:5] offset:49152
	s_setprio 1
	s_waitcnt lgkmcnt(1)
	v_mfma_f32_16x16x32_f16 v[0:3], v[12:15], v[170:173], v[0:3]
	v_mfma_f32_16x16x32_f16 v[4:7], v[12:15], v[174:177], v[8:11]
	v_mfma_f32_16x16x32_f16 v[8:11], v[12:15], v[178:181], v[52:55]
	v_mfma_f32_16x16x32_f16 v[12:15], v[12:15], v[182:185], v[80:83]
	v_mfma_f32_16x16x32_f16 v[16:19], v[40:43], v[170:173], v[92:95]
	v_mfma_f32_16x16x32_f16 v[20:23], v[40:43], v[174:177], v[102:105]
	v_mfma_f32_16x16x32_f16 v[36:39], v[40:43], v[178:181], v[106:109]
	v_mfma_f32_16x16x32_f16 v[40:43], v[40:43], v[182:185], v[110:113]
	s_setprio 0
	ds_read_b128 v[52:55], v130 offset:4096
	ds_read_b128 v[72:75], v130 offset:6144
	v_cvt_pk_f16_f32 v27, v26, v27
	v_cvt_pk_f16_f32 v26, v24, v25
	ds_write_b64 v100, v[26:27] offset:53248
	s_setprio 1
	s_waitcnt lgkmcnt(1)
	v_mfma_f32_16x16x32_f16 v[24:27], v[52:55], v[170:173], v[190:193]
	v_mfma_f32_16x16x32_f16 v[44:47], v[52:55], v[174:177], v[56:59]
	v_mfma_f32_16x16x32_f16 v[48:51], v[52:55], v[178:181], v[64:67]
	v_mfma_f32_16x16x32_f16 v[52:55], v[52:55], v[182:185], v[68:71]
	v_mfma_f32_16x16x32_f16 v[56:59], v[72:75], v[170:173], v[84:87]
	v_mfma_f32_16x16x32_f16 v[60:63], v[72:75], v[174:177], v[96:99]
	v_mfma_f32_16x16x32_f16 v[64:67], v[72:75], v[178:181], v[114:117]
	v_mfma_f32_16x16x32_f16 v[68:71], v[72:75], v[182:185], v[118:121]
	s_setprio 0
	ds_read_b128 v[80:83], v130 offset:8192
	ds_read_b128 v[96:99], v130 offset:10240
	v_cvt_pk_f16_f32 v31, v30, v31
	v_cvt_pk_f16_f32 v30, v28, v29
	ds_write_b64 v100, v[30:31] offset:57344
	s_setprio 1
	s_waitcnt lgkmcnt(1)
	v_mfma_f32_16x16x32_f16 v[28:31], v[80:83], v[170:173], v[122:125]
	v_mfma_f32_16x16x32_f16 v[72:75], v[80:83], v[174:177], v[186:189]
	v_mfma_f32_16x16x32_f16 v[76:79], v[80:83], v[178:181], v[202:205]
	v_mfma_f32_16x16x32_f16 v[80:83], v[80:83], v[182:185], v[88:91]
	v_mfma_f32_16x16x32_f16 v[84:87], v[96:99], v[170:173], v[134:137]
	v_mfma_f32_16x16x32_f16 v[88:91], v[96:99], v[174:177], v[138:141]
	v_mfma_f32_16x16x32_f16 v[92:95], v[96:99], v[178:181], v[146:149]
	v_mfma_f32_16x16x32_f16 v[96:99], v[96:99], v[182:185], v[142:145]
	s_setprio 0
	ds_read_b128 v[108:111], v130 offset:12288
	ds_read_b128 v[124:127], v130 offset:14336
	v_cvt_pk_f16_f32 v35, v34, v35
	v_cvt_pk_f16_f32 v34, v32, v33
	ds_write_b64 v100, v[34:35] offset:61440
	s_setprio 1
	s_waitcnt lgkmcnt(1)
	v_mfma_f32_16x16x32_f16 v[32:35], v[108:111], v[170:173], v[206:209]
	v_mfma_f32_16x16x32_f16 v[100:103], v[108:111], v[174:177], v[210:213]
	v_mfma_f32_16x16x32_f16 v[104:107], v[108:111], v[178:181], v[214:217]
	v_mfma_f32_16x16x32_f16 v[108:111], v[108:111], v[182:185], v[150:153]
	v_mfma_f32_16x16x32_f16 v[112:115], v[124:127], v[170:173], v[154:157]
	v_mfma_f32_16x16x32_f16 v[116:119], v[124:127], v[174:177], v[158:161]
	v_mfma_f32_16x16x32_f16 v[120:123], v[124:127], v[178:181], v[166:169]
	v_mfma_f32_16x16x32_f16 v[124:127], v[124:127], v[182:185], v[162:165]
	s_setprio 0
	s_waitcnt vmcnt(0)
	s_waitcnt lgkmcnt(0)
	s_barrier
	ds_read_b128 v[134:137], v131 offset:32768
	ds_read_b128 v[138:141], v131 offset:34816
	ds_read_b128 v[142:145], v131 offset:36864
	ds_read_b128 v[148:151], v131 offset:38912
	ds_read_b128 v[152:155], v129 offset:32768
	ds_read_b128 v[156:159], v129 offset:34816
	s_setprio 1
	s_waitcnt lgkmcnt(0)
	v_mfma_f32_16x16x32_f16 v[0:3], v[152:155], v[134:137], v[0:3]
	v_mfma_f32_16x16x32_f16 v[4:7], v[152:155], v[138:141], v[4:7]
	v_mfma_f32_16x16x32_f16 v[8:11], v[152:155], v[142:145], v[8:11]
	v_mfma_f32_16x16x32_f16 v[12:15], v[152:155], v[148:151], v[12:15]
	v_mfma_f32_16x16x32_f16 v[16:19], v[156:159], v[134:137], v[16:19]
	v_mfma_f32_16x16x32_f16 v[20:23], v[156:159], v[138:141], v[20:23]
	v_mfma_f32_16x16x32_f16 v[36:39], v[156:159], v[142:145], v[36:39]
	v_mfma_f32_16x16x32_f16 v[40:43], v[156:159], v[148:151], v[40:43]
	s_setprio 0
	ds_read_b128 v[152:155], v129 offset:36864
	ds_read_b128 v[156:159], v129 offset:38912
	v_and_b32_e32 v250, 0x7ffffc00, v194
	v_lshl_add_u64 v[252:253], s[10:11], 0, v[196:197]
	v_readfirstlane_b32 s32, v250
	s_nop 0
	s_mov_b32 m0, s32
	s_nop 0
	global_load_lds_dwordx4 v[252:253], off
	v_mov_b32_e32 v146, 0
	v_and_b32_e32 v251, 0xfffffff, v132
	v_cmp_gt_u32_e32 vcc, s82, v251
	v_mov_b32_e32 v132, 0
	v_mov_b32_e32 v133, 0
	s_and_saveexec_b64 s[0:1], vcc
	s_cbranch_execz .LBB1_7
	s_and_b32 s64, s78, 0x7ffffc00
	s_or_b32 s64, s64, s33
	v_or_b32_e32 v132, s64, v251
	v_mov_b32_e32 v133, v195
	v_lshl_add_u64 v[132:133], v[132:133], 2, s[12:13]
	global_load_dword v133, v[132:133], off
	v_or_b32_e32 v132, s33, v251
	v_lshlrev_b32_e32 v132, 2, v132
	global_load_dword v146, v132, s[16:17]
	s_nop 0
	global_load_dword v132, v132, s[14:15]
